# attention: K rows fed to the QK MFMA with row bits 2,3 swapped so P needs no permlane32 swaps before the PV MFMA (mask offsets adjusted), on top of v26
# baseline (speedup 1.0000x reference)
.LBB0_804:
	s_bfe_u32 s0, s66, 0x20001
	s_bfe_u32 s1, s78, 0x10007
	s_lshl_b32 s12, s1, 8
	s_lshl_b32 s44, s0, 9
	s_or_b32 s48, s44, s12
	s_mulk_i32 s0, 0x180
	s_mul_i32 s12, s1, 0xc0
	s_add_i32 s0, s0, s12
	s_lshl_b32 s50, s0, 1
	s_ashr_i32 s0, s78, 4
	s_lshl_b32 s12, s78, 1
	s_and_b32 s0, s0, -16
	s_and_b32 s44, s12, 8
	s_bfe_u32 s80, s78, 0x40003
	s_or_b32 s0, s0, s44
	s_xor_b32 s49, s80, 31
	s_ashr_i32 s0, s0, 3
	s_and_b32 s12, s12, 6
	s_lshl_b32 s83, s49, 8
	s_or_b32 s46, s12, s1
	s_ashr_i32 s1, s0, 31
	s_add_i32 s84, s83, s63
	s_lshr_b32 s81, s78, 3
	v_mov_b32_e32 v172, v1
	s_lshl_b64 s[52:53], s[0:1], 13
	s_ashr_i32 s12, s84, 31
	s_add_u32 s54, s52, s84
	v_and_b32_e32 v168, 31, v172
	v_or_b32_e32 v38, s54, v168
	s_addc_u32 s55, s53, s12
	v_mad_u64_u32 v[2:3], s[44:45], v38, s68, v[146:147]
	s_mul_i32 s82, s46, 0xc0
	v_bfe_u32 v173, v172, 5, 1
	v_mad_i32_i24 v3, s55, v162, v3
	s_lshl_b32 s12, s82, 1
	v_lshl_add_u64 v[2:3], v[2:3], 0, s[12:13]
	v_lshlrev_b32_e32 v148, 4, v173
	v_lshl_add_u64 v[40:41], v[2:3], 0, v[148:149]
	global_load_dwordx4 v[6:9], v[40:41], off
	global_load_dwordx4 v[14:17], v[40:41], off offset:32
	global_load_dwordx4 v[30:33], v[40:41], off offset:64
	global_load_dwordx4 v[34:37], v[40:41], off offset:96
	global_load_dwordx4 v[50:53], v[40:41], off offset:128
	global_load_dwordx4 v[26:29], v[40:41], off offset:160
	global_load_dwordx4 v[22:25], v[40:41], off offset:192
	global_load_dwordx4 v[18:21], v[40:41], off offset:224
	global_load_dwordx4 v[10:13], v[40:41], off offset:256
	global_load_dwordx4 v[42:45], v[40:41], off offset:288
	s_waitcnt lgkmcnt(0)
	global_load_dwordx4 v[2:5], v[40:41], off offset:320
	global_load_dwordx4 v[46:49], v[40:41], off offset:352
	v_and_b32_e32 v40, 32, v172
	v_mov_b32_e32 v39, s55
	s_mul_i32 s86, s0, 0x1800000
	s_mul_hi_i32 s51, s0, 0x1800000
	s_add_u32 s44, s33, s86
	s_addc_u32 s45, s58, s51
	s_lshl_b64 s[56:57], s[0:1], 24
	s_lshl_b32 s79, s46, 7
	s_add_u32 s44, s44, s12
	s_addc_u32 s45, s45, 0
	s_mov_b32 m0, s71
	s_add_u32 s0, s59, s56
	s_addc_u32 s1, s60, s57
	s_lshl_b32 s12, s46, 8
	s_add_u32 s46, s0, s12
	s_addc_u32 s47, s1, 0
	s_lshl_b32 s85, s49, 2
	s_add_i32 s85, s85, 4
	s_or_b32 s48, s56, s48
	s_add_u32 s48, s48, 0x29020000
	s_addc_u32 s49, s57, 0
	s_or_b32 s50, s86, s50
	s_add_u32 s50, s50, 0x23030000
	s_addc_u32 s51, s51, 0
	s_mov_b32 s12, 1
	s_movk_i32 s86, 0xff00
	s_waitcnt vmcnt(0)
	v_lshlrev_b32_e32 v227, 16, v26
	v_lshlrev_b32_e32 v177, 16, v6
	v_and_b32_e32 v174, 0xffff0000, v6
	v_lshlrev_b32_e32 v170, 16, v7
	v_and_b32_e32 v167, 0xffff0000, v7
	v_lshlrev_b32_e32 v180, 16, v8
	v_and_b32_e32 v176, 0xffff0000, v8
	v_lshlrev_b32_e32 v171, 16, v9
	v_and_b32_e32 v169, 0xffff0000, v9
	v_lshlrev_b32_e32 v185, 16, v14
	v_and_b32_e32 v182, 0xffff0000, v14
	v_lshlrev_b32_e32 v179, 16, v15
	v_and_b32_e32 v175, 0xffff0000, v15
	v_lshlrev_b32_e32 v187, 16, v16
	v_and_b32_e32 v183, 0xffff0000, v16
	v_lshlrev_b32_e32 v181, 16, v17
	v_and_b32_e32 v178, 0xffff0000, v17
	v_lshlrev_b32_e32 v201, 16, v34
	v_and_b32_e32 v198, 0xffff0000, v34
	v_lshlrev_b32_e32 v196, 16, v35
	v_and_b32_e32 v192, 0xffff0000, v35
	v_lshlrev_b32_e32 v202, 16, v36
	v_and_b32_e32 v199, 0xffff0000, v36
	v_lshlrev_b32_e32 v197, 16, v37
	v_and_b32_e32 v194, 0xffff0000, v37
	v_and_b32_e32 v228, 0xffff0000, v26
	global_load_dwordx4 v[142:145], v40, s[4:5] offset:704
	global_load_dwordx4 v[130:133], v40, s[4:5] offset:720
	global_load_dwordx4 v[6:9], v40, s[4:5] offset:592
	v_lshlrev_b32_e32 v229, 16, v27
	global_load_dwordx4 v[14:17], v40, s[4:5] offset:576
	v_and_b32_e32 v230, 0xffff0000, v27
	v_lshlrev_b32_e32 v231, 16, v28
	v_and_b32_e32 v232, 0xffff0000, v28
	v_lshlrev_b32_e32 v233, 16, v29
	v_and_b32_e32 v234, 0xffff0000, v29
	global_load_dwordx4 v[34:37], v40, s[4:5] offset:640
	global_load_dwordx4 v[156:159], v40, s[4:5] offset:656
	global_load_dwordx4 v[26:29], v40, s[4:5] offset:528
	v_mul_f32_e32 v209, v174, v174
	v_fmac_f32_e32 v209, v177, v177
	v_fmac_f32_e32 v209, v170, v170
	v_fmac_f32_e32 v209, v167, v167
	v_fmac_f32_e32 v209, v180, v180
	v_fmac_f32_e32 v209, v176, v176
	v_fmac_f32_e32 v209, v171, v171
	v_fmac_f32_e32 v209, v169, v169
	v_fmac_f32_e32 v209, v185, v185
	v_lshlrev_b32_e32 v193, 16, v30
	v_and_b32_e32 v190, 0xffff0000, v30
	v_lshlrev_b32_e32 v188, 16, v31
	v_and_b32_e32 v184, 0xffff0000, v31
	v_lshlrev_b32_e32 v195, 16, v32
	v_and_b32_e32 v191, 0xffff0000, v32
	v_lshlrev_b32_e32 v189, 16, v33
	v_and_b32_e32 v186, 0xffff0000, v33
	v_fmac_f32_e32 v209, v182, v182
	global_load_dwordx4 v[30:33], v40, s[4:5] offset:512
	v_fmac_f32_e32 v209, v179, v179
	v_fmac_f32_e32 v209, v175, v175
	v_fmac_f32_e32 v209, v187, v187
	v_fmac_f32_e32 v209, v183, v183
	v_fmac_f32_e32 v209, v181, v181
	v_fmac_f32_e32 v209, v178, v178
	v_fmac_f32_e32 v209, v193, v193
	v_fmac_f32_e32 v209, v190, v190
	v_fmac_f32_e32 v209, v188, v188
	v_fmac_f32_e32 v209, v184, v184
	v_fmac_f32_e32 v209, v195, v195
	v_fmac_f32_e32 v209, v191, v191
	v_fmac_f32_e32 v209, v189, v189
	v_fmac_f32_e32 v209, v186, v186
	v_fmac_f32_e32 v209, v201, v201
	v_fmac_f32_e32 v209, v198, v198
	v_fmac_f32_e32 v209, v196, v196
	v_fmac_f32_e32 v209, v192, v192
	v_fmac_f32_e32 v209, v202, v202
	v_fmac_f32_e32 v209, v199, v199
	v_fmac_f32_e32 v209, v197, v197
	v_lshlrev_b32_e32 v207, 16, v50
	v_fmac_f32_e32 v209, v194, v194
	v_and_b32_e32 v205, 0xffff0000, v50
	v_fmac_f32_e32 v209, v207, v207
	v_lshlrev_b32_e32 v203, 16, v51
	v_fmac_f32_e32 v209, v205, v205
	v_and_b32_e32 v200, 0xffff0000, v51
	v_fmac_f32_e32 v209, v203, v203
	v_lshlrev_b32_e32 v208, 16, v52
	v_fmac_f32_e32 v209, v200, v200
	v_and_b32_e32 v206, 0xffff0000, v52
	v_fmac_f32_e32 v209, v208, v208
	v_lshlrev_b32_e32 v204, 16, v53
	v_fmac_f32_e32 v209, v206, v206
	v_and_b32_e32 v226, 0xffff0000, v53
	v_fmac_f32_e32 v209, v204, v204
	v_fmac_f32_e32 v209, v226, v226
	v_fmac_f32_e32 v209, v227, v227
	v_fmac_f32_e32 v209, v228, v228
	v_fmac_f32_e32 v209, v229, v229
	v_fmac_f32_e32 v209, v230, v230
	global_load_dwordx4 v[110:113], v40, s[4:5] offset:16
	global_load_dwordx4 v[114:117], v40, s[4:5]
	global_load_dwordx4 v[102:105], v40, s[4:5] offset:80
	global_load_dwordx4 v[106:109], v40, s[4:5] offset:64
	global_load_dwordx4 v[94:97], v40, s[4:5] offset:144
	global_load_dwordx4 v[98:101], v40, s[4:5] offset:128
	global_load_dwordx4 v[86:89], v40, s[4:5] offset:208
	global_load_dwordx4 v[90:93], v40, s[4:5] offset:192
	global_load_dwordx4 v[78:81], v40, s[4:5] offset:272
	global_load_dwordx4 v[82:85], v40, s[4:5] offset:256
	global_load_dwordx4 v[70:73], v40, s[4:5] offset:336
	global_load_dwordx4 v[74:77], v40, s[4:5] offset:320
	global_load_dwordx4 v[62:65], v40, s[4:5] offset:400
	global_load_dwordx4 v[66:69], v40, s[4:5] offset:384
	global_load_dwordx4 v[54:57], v40, s[4:5] offset:464
	global_load_dwordx4 v[58:61], v40, s[4:5] offset:448
	v_fmac_f32_e32 v209, v231, v231
	v_fmac_f32_e32 v209, v232, v232
	v_fmac_f32_e32 v209, v233, v233
	v_fmac_f32_e32 v209, v234, v234
	s_waitcnt vmcnt(29)
	v_lshlrev_b32_e32 v235, 16, v22
	v_and_b32_e32 v236, 0xffff0000, v22
	v_fmac_f32_e32 v209, v235, v235
	v_lshlrev_b32_e32 v237, 16, v23
	v_fmac_f32_e32 v209, v236, v236
	v_and_b32_e32 v238, 0xffff0000, v23
	v_fmac_f32_e32 v209, v237, v237
	v_lshlrev_b32_e32 v239, 16, v24
	v_fmac_f32_e32 v209, v238, v238
	v_and_b32_e32 v240, 0xffff0000, v24
	v_fmac_f32_e32 v209, v239, v239
	v_lshlrev_b32_e32 v241, 16, v25
	v_fmac_f32_e32 v209, v240, v240
	v_and_b32_e32 v242, 0xffff0000, v25
	v_fmac_f32_e32 v209, v241, v241
	v_fmac_f32_e32 v209, v242, v242
	s_waitcnt vmcnt(28)
	v_lshlrev_b32_e32 v243, 16, v18
	v_and_b32_e32 v244, 0xffff0000, v18
	v_fmac_f32_e32 v209, v243, v243
	v_lshlrev_b32_e32 v245, 16, v19
	v_fmac_f32_e32 v209, v244, v244
	v_and_b32_e32 v246, 0xffff0000, v19
	v_fmac_f32_e32 v209, v245, v245
	v_lshlrev_b32_e32 v247, 16, v20
	v_fmac_f32_e32 v209, v246, v246
	v_and_b32_e32 v248, 0xffff0000, v20
	v_fmac_f32_e32 v209, v247, v247
	v_lshlrev_b32_e32 v249, 16, v21
	v_fmac_f32_e32 v209, v248, v248
	v_and_b32_e32 v250, 0xffff0000, v21
	v_fmac_f32_e32 v209, v249, v249
	s_waitcnt vmcnt(27)
	v_lshlrev_b32_e32 v223, 16, v10
	s_waitcnt vmcnt(25)
	v_lshlrev_b32_e32 v222, 16, v2
	v_fmac_f32_e32 v209, v250, v250
	s_waitcnt vmcnt(18)
	v_mov_b32_e32 v150, v158
	v_mov_b32_e32 v158, v156
	v_lshlrev_b32_e32 v156, 16, v3
	v_and_b32_e32 v160, 0xffff0000, v3
	v_and_b32_e32 v225, 0xffff0000, v10
	v_and_b32_e32 v224, 0xffff0000, v2
	v_pk_mul_f32 v[2:3], v[222:223], v[222:223]
	v_mov_b32_e32 v134, v144
	v_mov_b32_e32 v140, v142
	v_lshlrev_b32_e32 v142, 16, v5
	s_waitcnt vmcnt(17)
	v_mov_b32_e32 v151, v28
	v_and_b32_e32 v144, 0xffff0000, v5
	v_mov_b32_e32 v28, v159
	v_lshlrev_b32_e32 v152, 16, v4
	v_mov_b32_e32 v159, v26
	v_and_b32_e32 v154, 0xffff0000, v4
	v_mov_b32_e32 v26, v157
	v_lshlrev_b32_e32 v157, 16, v11
	v_add_f32_e32 v3, v3, v209
	v_pk_mul_f32 v[4:5], v[224:225], v[224:225]
	v_lshlrev_b32_e32 v119, 16, v45
	v_and_b32_e32 v121, 0xffff0000, v45
	v_lshlrev_b32_e32 v125, 16, v44
	v_and_b32_e32 v127, 0xffff0000, v44
	v_pk_mul_f32 v[44:45], v[156:157], v[156:157]
	v_and_b32_e32 v161, 0xffff0000, v11
	v_add_f32_e32 v3, v5, v3
	v_mov_b32_e32 v122, v132
	v_mov_b32_e32 v128, v130
	v_lshlrev_b32_e32 v130, 16, v47
	v_and_b32_e32 v132, 0xffff0000, v47
	v_lshlrev_b32_e32 v136, 16, v46
	v_and_b32_e32 v138, 0xffff0000, v46
	v_lshlrev_b32_e32 v153, 16, v12
	v_pk_mul_f32 v[46:47], v[160:161], v[160:161]
	v_add_f32_e32 v3, v45, v3
	v_mov_b32_e32 v123, v8
	v_mov_b32_e32 v8, v133
	v_mov_b32_e32 v129, v6
	v_mov_b32_e32 v6, v131
	v_lshlrev_b32_e32 v131, 16, v43
	v_and_b32_e32 v133, 0xffff0000, v43
	v_lshlrev_b32_e32 v137, 16, v42
	v_and_b32_e32 v139, 0xffff0000, v42
	v_pk_mul_f32 v[42:43], v[152:153], v[152:153]
	v_and_b32_e32 v155, 0xffff0000, v12
	v_add_f32_e32 v3, v47, v3
	v_mov_b32_e32 v141, v14
	v_mov_b32_e32 v14, v143
	v_lshlrev_b32_e32 v143, 16, v13
	v_pk_mul_f32 v[220:221], v[154:155], v[154:155]
	v_add_f32_e32 v3, v43, v3
	v_mov_b32_e32 v135, v16
	v_mov_b32_e32 v16, v145
	v_pk_mul_f32 v[216:217], v[142:143], v[142:143]
	v_and_b32_e32 v145, 0xffff0000, v13
	v_add_f32_e32 v3, v221, v3
	v_pk_mul_f32 v[218:219], v[144:145], v[144:145]
	v_add_f32_e32 v3, v217, v3
	v_pk_mul_f32 v[212:213], v[136:137], v[136:137]
	v_add_f32_e32 v3, v219, v3
	v_pk_mul_f32 v[214:215], v[138:139], v[138:139]
	v_add_f32_e32 v3, v213, v3
	v_add_f32_e32 v3, v215, v3
	v_fmac_f32_e32 v3, v131, v131
	v_fmac_f32_e32 v3, v133, v133
	v_fmac_f32_e32 v3, v125, v125
	v_fmac_f32_e32 v3, v127, v127
	v_fmac_f32_e32 v3, v119, v119
	v_fmac_f32_e32 v3, v121, v121
	v_add_f32_e32 v2, v2, v3
	v_add_f32_e32 v43, v4, v2
	v_add_f32_e32 v43, v44, v43
	v_add_f32_e32 v43, v46, v43
	v_add_f32_e32 v209, v42, v43
	v_add_f32_e32 v209, v220, v209
	v_add_f32_e32 v209, v216, v209
	v_add_f32_e32 v209, v218, v209
	v_mov_b32_e32 v218, v132
	v_mov_b32_e32 v219, v130
	v_add_f32_e32 v209, v212, v209
	v_lshlrev_b64 v[18:19], 8, v[38:39]
	v_lshlrev_b32_e32 v124, 16, v48
	v_and_b32_e32 v126, 0xffff0000, v48
	v_pk_mul_f32 v[218:219], v[218:219], v[218:219]
	s_waitcnt vmcnt(16)
	v_mov_b32_e32 v213, v32
	v_add_f32_e32 v32, v214, v209
	v_lshl_add_u64 v[18:19], s[10:11], 0, v[18:19]
	v_lshlrev_b32_e32 v20, 6, v173
	v_mov_b32_e32 v21, v149
	v_mov_b32_e32 v216, v126
	v_mov_b32_e32 v217, v124
	v_add_f32_e32 v32, v219, v32
	v_lshl_add_u64 v[210:211], v[18:19], 0, v[20:21]
	v_lshlrev_b32_e32 v118, 16, v49
	v_and_b32_e32 v120, 0xffff0000, v49
	v_pk_mul_f32 v[216:217], v[216:217], v[216:217]
	v_add_f32_e32 v32, v218, v32
	global_load_dwordx4 v[18:21], v[210:211], off offset:48
	global_load_dwordx4 v[22:25], v[210:211], off offset:32
	global_load_dwordx4 v[38:41], v[210:211], off offset:16
	global_load_dwordx4 v[50:53], v[210:211], off
	global_load_dwordx4 v[2:5], v[210:211], off offset:176
	global_load_dwordx4 v[10:13], v[210:211], off offset:160
	global_load_dwordx4 v[42:45], v[210:211], off offset:144
	global_load_dwordx4 v[46:49], v[210:211], off offset:128
	v_mov_b32_e32 v210, v120
	v_mov_b32_e32 v211, v118
	v_add_f32_e32 v32, v217, v32
	v_pk_mul_f32 v[210:211], v[210:211], v[210:211]
	v_add_f32_e32 v32, v216, v32
	v_add_f32_e32 v32, v211, v32
	v_add_f32_e32 v32, v210, v32
	v_mov_b32_e32 v212, v36
	v_mov_b32_e32 v36, v32
	s_nop 1
	v_permlane32_swap_b32_e32 v32, v36
	v_add_f32_e32 v32, v32, v36
	v_fmamk_f32 v32, v32, 0x3baaaaab, v163
	v_mul_f32_e32 v36, 0x4b800000, v32
	v_cmp_gt_f32_e32 vcc, s69, v32
	s_nop 1
	v_cndmask_b32_e32 v32, v32, v36, vcc
	v_rsq_f32_e32 v209, v32
	v_mov_b32_e32 v32, v37
	v_mov_b32_e32 v37, v30
	v_mov_b32_e32 v36, v34
	v_mul_f32_e32 v30, 0x45800000, v209
	v_cndmask_b32_e32 v30, v209, v30, vcc
	v_mul_f32_e32 v34, 0x3dd53b94, v30
	s_waitcnt vmcnt(22)
	v_mul_f32_e32 v30, v114, v34
	v_mul_f32_e32 v114, v30, v177
	v_mul_f32_e32 v30, v110, v34
	v_mul_f32_e32 v110, v30, v180
	v_mul_f32_e32 v30, v115, v34
	v_mul_f32_e32 v115, v30, v174
	v_mul_f32_e32 v30, v111, v34
	v_mul_f32_e32 v111, v30, v176
	v_mul_f32_e32 v30, v116, v34
	v_mul_f32_e32 v116, v30, v170
	v_mul_f32_e32 v30, v112, v34
	v_mul_f32_e32 v112, v30, v171
	v_mul_f32_e32 v30, v117, v34
	v_mul_f32_e32 v117, v30, v167
	v_mul_f32_e32 v30, v113, v34
	v_mul_f32_e32 v113, v30, v169
	s_waitcnt vmcnt(20)
	v_mul_f32_e32 v30, v106, v34
	v_mul_f32_e32 v106, v30, v185
	v_mul_f32_e32 v30, v102, v34
	v_mul_f32_e32 v167, v30, v187
	v_mul_f32_e32 v30, v107, v34
	v_mul_f32_e32 v102, v30, v182
	v_mul_f32_e32 v30, v103, v34
	v_mul_f32_e32 v107, v30, v183
	v_mul_f32_e32 v30, v108, v34
	v_mul_f32_e32 v103, v30, v179
	v_mul_f32_e32 v30, v104, v34
	v_mul_f32_e32 v108, v30, v181
	v_mul_f32_e32 v30, v109, v34
	v_mul_f32_e32 v104, v30, v175
	v_mul_f32_e32 v30, v105, v34
	v_mul_f32_e32 v105, v30, v178
	s_waitcnt vmcnt(18)
	v_mul_f32_e32 v30, v98, v34
	v_mul_f32_e32 v109, v30, v193
	v_mul_f32_e32 v30, v94, v34
	v_mul_f32_e32 v94, v30, v195
	v_mul_f32_e32 v30, v99, v34
	v_mul_f32_e32 v169, v30, v190
	v_mul_f32_e32 v30, v95, v34
	v_mul_f32_e32 v95, v30, v191
	v_mul_f32_e32 v30, v100, v34
	v_mul_f32_e32 v170, v30, v188
	v_mul_f32_e32 v30, v96, v34
	v_mul_f32_e32 v96, v30, v189
	v_mul_f32_e32 v30, v101, v34
	v_mul_f32_e32 v171, v30, v184
	v_mul_f32_e32 v30, v97, v34
	v_mul_f32_e32 v97, v30, v186
	s_waitcnt vmcnt(16)
	v_mul_f32_e32 v30, v90, v34
	v_mul_f32_e32 v90, v30, v201
	v_mul_f32_e32 v30, v86, v34
	v_mul_f32_e32 v86, v30, v202
	v_mul_f32_e32 v30, v91, v34
	v_mul_f32_e32 v91, v30, v198
	v_mul_f32_e32 v30, v87, v34
	v_mul_f32_e32 v87, v30, v199
	v_mul_f32_e32 v30, v92, v34
	v_mul_f32_e32 v92, v30, v196
	v_mul_f32_e32 v30, v88, v34
	v_mul_f32_e32 v88, v30, v197
	v_mul_f32_e32 v30, v93, v34
	v_mul_f32_e32 v93, v30, v192
	v_mul_f32_e32 v30, v89, v34
	v_mul_f32_e32 v89, v30, v194
	s_waitcnt vmcnt(14)
	v_mul_f32_e32 v30, v82, v34
	v_mul_f32_e32 v82, v30, v207
	v_mul_f32_e32 v30, v34, v78
	v_mul_f32_e32 v78, v30, v208
	v_mul_f32_e32 v30, v83, v34
	v_mul_f32_e32 v83, v30, v205
	v_mul_f32_e32 v30, v34, v79
	v_mul_f32_e32 v79, v30, v206
	v_mul_f32_e32 v30, v84, v34
	v_mul_f32_e32 v84, v30, v203
	v_mul_f32_e32 v30, v34, v80
	v_mul_f32_e32 v80, v30, v204
	v_mul_f32_e32 v30, v85, v34
	v_mul_f32_e32 v85, v30, v200
	v_mul_f32_e32 v30, v34, v81
	v_mul_f32_e32 v81, v30, v226
	s_waitcnt vmcnt(12)
	v_mul_f32_e32 v30, v34, v74
	v_mul_f32_e32 v74, v30, v227
	v_mul_f32_e32 v30, v34, v70
	v_mul_f32_e32 v70, v30, v231
	v_mul_f32_e32 v30, v34, v75
	v_mul_f32_e32 v75, v30, v228
	v_mul_f32_e32 v30, v34, v71
	v_mul_f32_e32 v71, v30, v232
	v_mul_f32_e32 v30, v34, v76
	v_mul_f32_e32 v76, v30, v229
	v_mul_f32_e32 v30, v34, v72
	v_mul_f32_e32 v72, v30, v233
	v_mul_f32_e32 v30, v34, v77
	v_mul_f32_e32 v77, v30, v230
	v_mul_f32_e32 v30, v34, v73
	v_mul_f32_e32 v73, v30, v234
	s_waitcnt vmcnt(10)
	v_mul_f32_e32 v30, v34, v66
	v_mul_f32_e32 v174, v30, v235
	v_mul_f32_e32 v30, v34, v62
	v_mul_f32_e32 v175, v30, v239
	v_mul_f32_e32 v30, v34, v67
	v_mul_f32_e32 v176, v30, v236
	v_mul_f32_e32 v30, v34, v63
	v_mul_f32_e32 v177, v30, v240
	v_mul_f32_e32 v30, v34, v68
	v_mul_f32_e32 v68, v30, v237
	v_mul_f32_e32 v30, v34, v64
	v_mul_f32_e32 v178, v30, v241
	v_mul_f32_e32 v30, v34, v69
	v_mul_f32_e32 v69, v30, v238
	v_mul_f32_e32 v30, v34, v65
	v_mul_f32_e32 v179, v30, v242
	s_waitcnt vmcnt(8)
	v_mul_f32_e32 v30, v34, v58
	v_mul_f32_e32 v180, v30, v243
	v_mul_f32_e32 v30, v34, v54
	v_mul_f32_e32 v181, v30, v247
	v_mul_f32_e32 v30, v34, v59
	v_mul_f32_e32 v182, v30, v244
	v_mul_f32_e32 v30, v34, v55
	v_mul_f32_e32 v183, v30, v248
	v_mul_f32_e32 v30, v34, v60
	v_mul_f32_e32 v184, v30, v245
	v_mul_f32_e32 v30, v34, v56
	v_mul_f32_e32 v185, v30, v249
	v_mul_f32_e32 v30, v34, v61
	v_mul_f32_e32 v186, v30, v246
	v_mul_f32_e32 v30, v34, v57
	v_pk_mul_f32 v[36:37], v[34:35], v[36:37] op_sel_hi:[0,1]
	v_mul_f32_e32 v187, v30, v250
	v_pk_mul_f32 v[36:37], v[36:37], v[222:223]
	v_mov_b32_e32 v30, v35
	v_pk_mul_f32 v[54:55], v[34:35], v[158:159] op_sel_hi:[0,1]
	v_pk_mul_f32 v[30:31], v[34:35], v[30:31] op_sel_hi:[0,1]
	v_pk_mul_f32 v[26:27], v[34:35], v[26:27] op_sel_hi:[0,1]
	v_pk_mul_f32 v[56:57], v[34:35], v[212:213] op_sel_hi:[0,1]
	v_pk_mul_f32 v[58:59], v[34:35], v[150:151] op_sel_hi:[0,1]
	v_pk_mul_f32 v[32:33], v[34:35], v[32:33] op_sel_hi:[0,1]
	v_pk_mul_f32 v[28:29], v[34:35], v[28:29] op_sel_hi:[0,1]
	v_pk_mul_f32 v[60:61], v[34:35], v[140:141] op_sel_hi:[0,1]
	v_pk_mul_f32 v[62:63], v[34:35], v[128:129] op_sel_hi:[0,1]
	v_pk_mul_f32 v[14:15], v[34:35], v[14:15] op_sel_hi:[0,1]
	v_pk_mul_f32 v[6:7], v[34:35], v[6:7] op_sel_hi:[0,1]
	v_pk_mul_f32 v[64:65], v[34:35], v[134:135] op_sel_hi:[0,1]
	v_pk_mul_f32 v[66:67], v[34:35], v[122:123] op_sel_hi:[0,1]
	v_pk_mul_f32 v[16:17], v[34:35], v[16:17] op_sel_hi:[0,1]
	v_pk_mul_f32 v[8:9], v[34:35], v[8:9] op_sel_hi:[0,1]
	s_waitcnt vmcnt(4)
	v_pk_mul_f32 v[34:35], v[36:37], v[50:51] op_sel:[1,0] op_sel_hi:[0,1]
	v_pk_mul_f32 v[30:31], v[30:31], v[224:225]
	v_pk_mul_f32 v[64:65], v[64:65], v[130:131]
	v_sub_f32_e32 v130, v34, v35
	v_pk_mul_f32 v[34:35], v[36:37], v[50:51]
	v_pk_mul_f32 v[56:57], v[56:57], v[156:157]
	v_add_f32_e32 v36, v35, v34
	v_pk_mul_f32 v[34:35], v[30:31], v[52:53] op_sel:[1,0] op_sel_hi:[0,1]
	v_pk_mul_f32 v[30:31], v[30:31], v[52:53]
	v_sub_f32_e32 v34, v34, v35
	v_add_f32_e32 v35, v31, v30
	v_pk_mul_f32 v[30:31], v[56:57], v[38:39] op_sel:[1,0] op_sel_hi:[0,1]
	v_pk_mul_f32 v[32:33], v[32:33], v[160:161]
	v_sub_f32_e32 v37, v30, v31
	v_pk_mul_f32 v[30:31], v[56:57], v[38:39]
	v_pk_mul_f32 v[54:55], v[54:55], v[152:153]
	v_add_f32_e32 v38, v31, v30
	v_pk_mul_f32 v[30:31], v[32:33], v[40:41] op_sel:[1,0] op_sel_hi:[0,1]
	v_sub_f32_e32 v39, v30, v31
	v_pk_mul_f32 v[30:31], v[32:33], v[40:41]
	v_pk_mul_f32 v[26:27], v[26:27], v[154:155]
	v_add_f32_e32 v32, v31, v30
	v_pk_mul_f32 v[30:31], v[54:55], v[22:23] op_sel:[1,0] op_sel_hi:[0,1]
	v_pk_mul_f32 v[22:23], v[54:55], v[22:23]
	v_sub_f32_e32 v30, v30, v31
	v_add_f32_e32 v31, v23, v22
	v_pk_mul_f32 v[22:23], v[26:27], v[24:25] op_sel:[1,0] op_sel_hi:[0,1]
	v_pk_mul_f32 v[58:59], v[58:59], v[142:143]
	v_sub_f32_e32 v33, v22, v23
	v_pk_mul_f32 v[22:23], v[26:27], v[24:25]
	v_pk_mul_f32 v[28:29], v[28:29], v[144:145]
	v_add_f32_e32 v24, v23, v22
	v_pk_mul_f32 v[22:23], v[58:59], v[18:19] op_sel:[1,0] op_sel_hi:[0,1]
	v_pk_mul_f32 v[18:19], v[58:59], v[18:19]
	v_sub_f32_e32 v22, v22, v23
	v_add_f32_e32 v23, v19, v18
	v_pk_mul_f32 v[18:19], v[28:29], v[20:21] op_sel:[1,0] op_sel_hi:[0,1]
	v_pk_mul_f32 v[60:61], v[60:61], v[136:137]
	v_sub_f32_e32 v25, v18, v19
	v_pk_mul_f32 v[18:19], v[28:29], v[20:21]
	v_pk_mul_f32 v[14:15], v[14:15], v[138:139]
	v_add_f32_e32 v20, v19, v18
	s_waitcnt vmcnt(0)
	v_pk_mul_f32 v[18:19], v[60:61], v[46:47] op_sel:[1,0] op_sel_hi:[0,1]
	v_sub_f32_e32 v21, v18, v19
	v_pk_mul_f32 v[18:19], v[60:61], v[46:47]
	v_pk_mul_f32 v[16:17], v[16:17], v[132:133]
	v_add_f32_e32 v26, v19, v18
	v_pk_mul_f32 v[18:19], v[14:15], v[48:49] op_sel:[1,0] op_sel_hi:[0,1]
	v_pk_mul_f32 v[14:15], v[14:15], v[48:49]
	v_sub_f32_e32 v18, v18, v19
	v_add_f32_e32 v19, v15, v14
	v_pk_mul_f32 v[14:15], v[64:65], v[42:43] op_sel:[1,0] op_sel_hi:[0,1]
	v_sub_f32_e32 v27, v14, v15
	v_pk_mul_f32 v[14:15], v[64:65], v[42:43]
	v_pk_mul_f32 v[62:63], v[62:63], v[124:125]
	v_add_f32_e32 v28, v15, v14
	v_pk_mul_f32 v[14:15], v[16:17], v[44:45] op_sel:[1,0] op_sel_hi:[0,1]
	v_sub_f32_e32 v29, v14, v15
	v_pk_mul_f32 v[14:15], v[16:17], v[44:45]
	v_pk_mul_f32 v[6:7], v[6:7], v[126:127]
	v_add_f32_e32 v16, v15, v14
	v_pk_mul_f32 v[14:15], v[62:63], v[10:11] op_sel:[1,0] op_sel_hi:[0,1]
	v_pk_mul_f32 v[10:11], v[62:63], v[10:11]
	v_pk_mul_f32 v[66:67], v[66:67], v[118:119]
	v_sub_f32_e32 v14, v14, v15
	v_add_f32_e32 v15, v11, v10
	v_pk_mul_f32 v[10:11], v[6:7], v[12:13] op_sel:[1,0] op_sel_hi:[0,1]
	v_pk_mul_f32 v[6:7], v[6:7], v[12:13]
	v_pk_mul_f32 v[8:9], v[8:9], v[120:121]
	v_sub_f32_e32 v10, v10, v11
	v_add_f32_e32 v11, v7, v6
	v_pk_mul_f32 v[6:7], v[66:67], v[2:3] op_sel:[1,0] op_sel_hi:[0,1]
	v_pk_mul_f32 v[2:3], v[66:67], v[2:3]
	v_sub_f32_e32 v6, v6, v7
	v_add_f32_e32 v7, v3, v2
	v_pk_mul_f32 v[2:3], v[8:9], v[4:5] op_sel:[1,0] op_sel_hi:[0,1]
	v_sub_f32_e32 v12, v2, v3
	v_pk_mul_f32 v[2:3], v[8:9], v[4:5]
	v_cvt_pk_bf16_f32 v98, v114, v115
	v_cvt_pk_bf16_f32 v99, v116, v117
	v_cvt_pk_bf16_f32 v100, v110, v111
	v_cvt_pk_bf16_f32 v101, v112, v113
	v_cvt_pk_bf16_f32 v102, v106, v102
	s_nop 0
	v_add_f32_e32 v2, v3, v2
	v_cvt_pk_bf16_f32 v103, v103, v104
	v_cvt_pk_bf16_f32 v104, v167, v107
	v_cvt_pk_bf16_f32 v105, v108, v105
	v_cvt_pk_bf16_f32 v106, v109, v169
	v_cvt_pk_bf16_f32 v107, v170, v171
	v_cvt_pk_bf16_f32 v108, v94, v95
	v_cvt_pk_bf16_f32 v109, v96, v97
	v_cvt_pk_bf16_f32 v110, v90, v91
	v_cvt_pk_bf16_f32 v111, v92, v93
	v_cvt_pk_bf16_f32 v112, v86, v87
	v_cvt_pk_bf16_f32 v113, v88, v89
	v_cvt_pk_bf16_f32 v114, v82, v83
	v_cvt_pk_bf16_f32 v115, v84, v85
	v_cvt_pk_bf16_f32 v116, v78, v79
	v_cvt_pk_bf16_f32 v117, v80, v81
	v_cvt_pk_bf16_f32 v118, v74, v75
	v_cvt_pk_bf16_f32 v119, v76, v77
	v_cvt_pk_bf16_f32 v120, v70, v71
	v_cvt_pk_bf16_f32 v121, v72, v73
	v_cvt_pk_bf16_f32 v122, v174, v176
	v_cvt_pk_bf16_f32 v123, v68, v69
	v_cvt_pk_bf16_f32 v124, v175, v177
	v_cvt_pk_bf16_f32 v125, v178, v179
	v_cvt_pk_bf16_f32 v126, v180, v182
	v_cvt_pk_bf16_f32 v127, v184, v186
	v_cvt_pk_bf16_f32 v128, v181, v183
	v_cvt_pk_bf16_f32 v129, v185, v187
	v_cvt_pk_bf16_f32 v130, v130, v34
	v_cvt_pk_bf16_f32 v131, v37, v39
	v_cvt_pk_bf16_f32 v132, v30, v33
	v_cvt_pk_bf16_f32 v133, v22, v25
	v_cvt_pk_bf16_f32 v134, v21, v18
	v_cvt_pk_bf16_f32 v135, v27, v29
	v_cvt_pk_bf16_f32 v136, v14, v10
	v_cvt_pk_bf16_f32 v137, v6, v12
	v_cvt_pk_bf16_f32 v138, v36, v35
	v_cvt_pk_bf16_f32 v139, v38, v32
	v_cvt_pk_bf16_f32 v140, v31, v24
	v_cvt_pk_bf16_f32 v141, v23, v20
	v_cvt_pk_bf16_f32 v142, v26, v19
	v_cvt_pk_bf16_f32 v143, v28, v16
	v_cvt_pk_bf16_f32 v144, v15, v11
	v_cvt_pk_bf16_f32 v145, v7, v2
	v_mul_hi_i32 v2, v172, s70
	v_lshrrev_b32_e32 v3, 31, v2
	v_ashrrev_i32_e32 v2, 2, v2
	v_add_u32_e32 v2, v2, v3
	v_mul_lo_u32 v3, v2, 24
	v_sub_u32_e32 v3, v172, v3
	v_lshrrev_b32_e32 v16, 1, v2
	v_bitop3_b32 v3, v16, v3, 7 bitop3:0x6c
	v_mul_lo_u32 v2, v2, s68
	v_lshl_add_u32 v2, v3, 4, v2
	v_add_u32_e32 v3, 0x200, v172
	v_mul_hi_i32 v4, v3, s70
	v_lshrrev_b32_e32 v5, 31, v4
	v_ashrrev_i32_e32 v4, 2, v4
	v_add_u32_e32 v4, v4, v5
	v_mul_lo_u32 v5, v4, 24
	v_sub_u32_e32 v5, v3, v5
	v_lshrrev_b32_e32 v16, 1, v4
	v_bitop3_b32 v5, v16, v5, 7 bitop3:0x6c
	v_mul_lo_u32 v4, v4, s68
	v_lshl_add_u32 v4, v5, 4, v4
	v_add_u32_e32 v5, 0x400, v172
	v_mul_hi_i32 v6, v5, s70
	v_lshrrev_b32_e32 v7, 31, v6
	v_ashrrev_i32_e32 v6, 2, v6
	v_add_u32_e32 v6, v6, v7
	v_mul_lo_u32 v7, v6, 24
	v_sub_u32_e32 v5, v5, v7
	v_lshrrev_b32_e32 v16, 1, v6
	v_bitop3_b32 v5, v16, v5, 7 bitop3:0x6c
	v_mul_lo_u32 v6, v6, s68
	v_ashrrev_i32_e32 v9, 4, v172
	v_lshl_add_u32 v6, v5, 4, v6
	v_bfe_u32 v5, v172, 2, 2
	v_lshrrev_b32_e32 v7, 1, v172
	v_and_b32_e32 v10, 0x1ffff0, v9
	v_lshrrev_b32_e32 v9, 1, v9
	v_ashrrev_i32_e32 v3, 4, v3
	v_and_or_b32 v5, v7, 8, v5
	v_and_b32_e32 v7, 0x60, v172
	v_lshlrev_b32_e32 v8, 3, v172
	v_and_b32_e32 v9, 4, v9
	v_and_b32_e32 v11, 0x1ffff0, v3
	v_lshrrev_b32_e32 v3, 1, v3
	v_and_or_b32 v7, v8, 24, v7
	v_or3_b32 v9, v10, v9, v5
	v_and_b32_e32 v3, 4, v3
	s_barrier
	global_load_lds_dwordx4 v2, s[44:45]
	s_mov_b32 m0, s72
	v_lshlrev_b32_e32 v7, 1, v7
	v_lshlrev_b32_e32 v10, 11, v9
	v_or3_b32 v3, v11, v3, v5
	global_load_lds_dwordx4 v4, s[44:45]
	s_mov_b32 m0, s73
	v_or_b32_e32 v9, v10, v7
	v_lshlrev_b32_e32 v11, 11, v3
	global_load_lds_dwordx4 v6, s[44:45]
	s_mov_b32 m0, s64
	v_or_b32_e32 v3, v11, v7
	global_load_lds_dwordx4 v9, s[46:47]
	s_mov_b32 m0, s74
	v_lshlrev_b32_e32 v13, 1, v172
	global_load_lds_dwordx4 v3, s[46:47]
	v_lshlrev_b32_e32 v9, 4, v172
	v_and_b32_e32 v14, 32, v13
	v_or_b32_e32 v3, 32, v148
	v_and_b32_e32 v16, 0x13, v168
	v_and_b32_e32 v17, 4, v168
	v_lshl_or_b32 v16, v17, 1, v16
	v_and_b32_e32 v17, 8, v168
	v_lshrrev_b32_e32 v17, 1, v17
	v_or_b32_e32 v16, v16, v17
	v_mul_u32_u24_e32 v5, 0x180, v16
	v_lshlrev_b32_e32 v17, 3, v16
	v_and_b32_e32 v7, 0x70, v17
	v_and_b32_e32 v12, 0xc0, v9
	v_and_or_b32 v8, v8, s75, v14
	v_and_b32_e32 v167, 63, v172
	v_bitop3_b32 v169, v3, v5, v7 bitop3:0xde
	v_or_b32_e32 v3, 64, v148
	v_add3_u32 v172, v12, 0, v8
	v_and_b32_e32 v12, 0xc0, v13
	v_and_b32_e32 v13, 48, v9
	v_bitop3_b32 v170, v3, v5, v7 bitop3:0xde
	v_or_b32_e32 v3, 0x60, v148
	v_or3_b32 v8, v11, v12, v13
	v_mov_b32_e32 v9, v149
	v_bitop3_b32 v161, v148, v5, v7 bitop3:0xde
	v_bitop3_b32 v171, v3, v5, v7 bitop3:0xde
	v_mov_b32_e32 v3, v149
	v_mov_b32_e32 v5, v149
	v_mov_b32_e32 v7, v149
	v_mul_i32_i24_e32 v15, -8, v173
	v_lshl_add_u64 v[150:151], s[48:49], 0, v[8:9]
	v_mov_b32_e32 v240, v8
	v_or3_b32 v8, v10, v12, v13
	v_mov_b32_e32 v16, v149
	v_mov_b32_e32 v17, v149
	v_lshl_add_u32 v160, v168, 2, s65
	v_lshl_add_u64 v[152:153], s[48:49], 0, v[8:9]
	v_mov_b32_e32 v241, v8
	v_lshl_add_u64 v[154:155], s[50:51], 0, v[6:7]
	v_mov_b32_e32 v242, v6
	v_lshl_add_u64 v[156:157], s[50:51], 0, v[4:5]
	v_mov_b32_e32 v243, v4
	v_lshl_add_u64 v[158:159], s[50:51], 0, v[2:3]
	v_mov_b32_e32 v244, v2
	s_add_u32 s94, s2, s50
	s_addc_u32 s95, s3, s51
	s_add_u32 s96, s2, s48
	s_addc_u32 s97, s3, s49
	v_add3_u32 v168, s63, v15, v168
	v_mov_b32_e32 v2, v149
	v_mov_b32_e32 v4, v149
	v_mov_b32_e32 v6, v149
	v_mov_b32_e32 v8, v149
	v_mov_b32_e32 v10, v149
	v_mov_b32_e32 v11, v149
	v_mov_b32_e32 v12, v149
	v_mov_b32_e32 v13, v149
	v_mov_b32_e32 v14, v149
	v_mov_b32_e32 v15, v149
	v_mov_b64_e32 v[32:33], v[16:17]
	v_mov_b64_e32 v[48:49], v[16:17]
	v_mov_b64_e32 v[64:65], v[16:17]
	v_cmp_gt_u32_e64 s[0:1], 32, v167
	v_mov_b32_e32 v173, 0
	v_mov_b32_e32 v206, 0
	v_mov_b32_e32 v207, 0
	v_mov_b32_e32 v208, 0
	v_mov_b32_e32 v209, 0
	v_mov_b32_e32 v210, 0
	v_mov_b32_e32 v211, 0
	v_mov_b32_e32 v212, 0
	v_mov_b32_e32 v213, 0
	v_mov_b32_e32 v214, 0
	v_mov_b32_e32 v215, 0
	v_mov_b32_e32 v216, 0
	v_mov_b32_e32 v217, 0
	v_mov_b32_e32 v218, 0
	v_mov_b32_e32 v219, 0
	v_mov_b32_e32 v220, 0
	v_mov_b32_e32 v221, 0
	v_mov_b64_e32 v[30:31], v[14:15]
	v_mov_b64_e32 v[28:29], v[12:13]
	v_mov_b64_e32 v[26:27], v[10:11]
	v_mov_b64_e32 v[24:25], v[8:9]
	v_mov_b64_e32 v[22:23], v[6:7]
	v_mov_b64_e32 v[20:21], v[4:5]
	v_mov_b64_e32 v[18:19], v[2:3]
	v_mov_b64_e32 v[46:47], v[14:15]
	v_mov_b64_e32 v[44:45], v[12:13]
	v_mov_b64_e32 v[42:43], v[10:11]
	v_mov_b64_e32 v[40:41], v[8:9]
	v_mov_b64_e32 v[38:39], v[6:7]
	v_mov_b64_e32 v[36:37], v[4:5]
	v_mov_b64_e32 v[34:35], v[2:3]
	v_mov_b64_e32 v[62:63], v[14:15]
	v_mov_b64_e32 v[60:61], v[12:13]
	v_mov_b64_e32 v[58:59], v[10:11]
	v_mov_b64_e32 v[56:57], v[8:9]
	v_mov_b64_e32 v[54:55], v[6:7]
	v_mov_b64_e32 v[52:53], v[4:5]
	v_mov_b64_e32 v[50:51], v[2:3]
	v_mov_b32_e32 v174, 0

.LBB0_807:
	s_mul_i32 s56, s87, 0x6000
	s_add_i32 s56, s56, 0
	s_add_i32 s56, s56, 0x8000
	v_add_u32_e32 v175, s56, v161
	ds_read_b128 v[66:69], v175 offset:0
	ds_read_b128 v[70:73], v175 offset:0x3000
	v_add_u32_e32 v200, s56, v169
	ds_read_b128 v[176:179], v200 offset:0
	ds_read_b128 v[180:183], v200 offset:0x3000
	v_add_u32_e32 v201, s56, v170
	ds_read_b128 v[184:187], v201 offset:0
	ds_read_b128 v[188:191], v201 offset:0x3000
	s_waitcnt lgkmcnt(4)
	v_add_u32_e32 v202, s56, v171
	v_mfma_f32_32x32x16_bf16 v[82:97], v[66:69], v[98:101], v[206:221]
	ds_read_b128 v[192:195], v202 offset:0
	ds_read_b128 v[196:199], v202 offset:0x3000
	s_waitcnt lgkmcnt(4)
	v_mfma_f32_32x32x16_bf16 v[66:81], v[70:73], v[98:101], v[206:221]
	v_mfma_f32_32x32x16_bf16 v[82:97], v[176:179], v[102:105], v[82:97]
	ds_read_b128 v[176:179], v175 offset:0x80
	v_mfma_f32_32x32x16_bf16 v[66:81], v[180:183], v[102:105], v[66:81]
	ds_read_b128 v[180:183], v175 offset:0x3080
	s_waitcnt lgkmcnt(4)
	v_mfma_f32_32x32x16_bf16 v[82:97], v[184:187], v[106:109], v[82:97]
	ds_read_b128 v[184:187], v200 offset:0x80
	v_mfma_f32_32x32x16_bf16 v[66:81], v[188:191], v[106:109], v[66:81]
	ds_read_b128 v[188:191], v200 offset:0x3080
	s_waitcnt lgkmcnt(4)
	v_mfma_f32_32x32x16_bf16 v[82:97], v[192:195], v[110:113], v[82:97]
	ds_read_b128 v[192:195], v201 offset:0x80
	v_mfma_f32_32x32x16_bf16 v[66:81], v[196:199], v[110:113], v[66:81]
	ds_read_b128 v[196:199], v201 offset:0x3080
	s_waitcnt lgkmcnt(4)
	v_mfma_f32_32x32x16_bf16 v[82:97], v[176:179], v[114:117], v[82:97]
	ds_read_b128 v[176:179], v202 offset:0x80
	v_mfma_f32_32x32x16_bf16 v[66:81], v[180:183], v[114:117], v[66:81]
	ds_read_b128 v[180:183], v202 offset:0x3080
	s_waitcnt lgkmcnt(4)
	v_mfma_f32_32x32x16_bf16 v[82:97], v[184:187], v[118:121], v[82:97]
	ds_read_b128 v[184:187], v175 offset:0x100
	v_mfma_f32_32x32x16_bf16 v[66:81], v[188:191], v[118:121], v[66:81]
	ds_read_b128 v[188:191], v175 offset:0x3100
	s_waitcnt lgkmcnt(4)
	v_mfma_f32_32x32x16_bf16 v[82:97], v[192:195], v[122:125], v[82:97]
	ds_read_b128 v[192:195], v200 offset:0x100
	v_mfma_f32_32x32x16_bf16 v[66:81], v[196:199], v[122:125], v[66:81]
	ds_read_b128 v[196:199], v200 offset:0x3100
	s_waitcnt lgkmcnt(4)
	v_mfma_f32_32x32x16_bf16 v[82:97], v[176:179], v[126:129], v[82:97]
	ds_read_b128 v[176:179], v201 offset:0x100
	v_mfma_f32_32x32x16_bf16 v[66:81], v[180:183], v[126:129], v[66:81]
	ds_read_b128 v[180:183], v201 offset:0x3100
	s_waitcnt lgkmcnt(4)
	v_mfma_f32_32x32x16_bf16 v[82:97], v[184:187], v[130:133], v[82:97]
	ds_read_b128 v[184:187], v202 offset:0x100
	v_mfma_f32_32x32x16_bf16 v[66:81], v[188:191], v[130:133], v[66:81]
	ds_read_b128 v[188:191], v202 offset:0x3100
	s_waitcnt lgkmcnt(4)
	v_mfma_f32_32x32x16_bf16 v[82:97], v[192:195], v[134:137], v[82:97]
	s_waitcnt lgkmcnt(2)
	v_mfma_f32_32x32x16_bf16 v[66:81], v[196:199], v[134:137], v[66:81]
	v_mfma_f32_32x32x16_bf16 v[82:97], v[176:179], v[138:141], v[82:97]
	s_waitcnt lgkmcnt(0)
	v_mfma_f32_32x32x16_bf16 v[66:81], v[180:183], v[138:141], v[66:81]
	v_mfma_f32_32x32x16_bf16 v[82:97], v[184:187], v[142:145], v[82:97]
	s_add_i32 s56, s86, 0x13f
	s_cmp_le_i32 s56, s84
	v_mfma_f32_32x32x16_bf16 v[66:81], v[188:191], v[142:145], v[66:81]
	s_cbranch_scc1 .LBB0_809
	v_add_u32_e32 v175, s83, v168
	v_cmp_lt_i32_e32 vcc, -1, v175
	v_add_u32_e32 v176, -1, v175
	s_nop 4
	v_cndmask_b32_e32 v82, v165, v82, vcc
	v_cmp_lt_i32_e32 vcc, 31, v175
	s_nop 1
	v_cndmask_b32_e32 v66, v165, v66, vcc
	v_cmp_lt_i32_e32 vcc, -1, v176
	s_nop 1
	v_cndmask_b32_e32 v83, v165, v83, vcc
	v_cmp_lt_i32_e32 vcc, 31, v176
	v_add_u32_e32 v176, -2, v175
	s_nop 0
	v_cndmask_b32_e32 v67, v165, v67, vcc
	v_cmp_lt_i32_e32 vcc, -1, v176
	s_nop 1
	v_cndmask_b32_e32 v84, v165, v84, vcc
	v_cmp_lt_i32_e32 vcc, 31, v176
	v_add_u32_e32 v176, -3, v175
	s_nop 0
	v_cndmask_b32_e32 v68, v165, v68, vcc
	v_cmp_lt_i32_e32 vcc, -1, v176
	s_nop 1
	v_cndmask_b32_e32 v85, v165, v85, vcc
	v_cmp_lt_i32_e32 vcc, 31, v176
	v_add_u32_e32 v176, -4, v175
	s_nop 0
	v_cndmask_b32_e32 v69, v165, v69, vcc
	v_cmp_lt_i32_e32 vcc, -1, v176
	s_nop 1
	v_cndmask_b32_e32 v86, v165, v86, vcc
	v_cmp_lt_i32_e32 vcc, 31, v176
	v_add_u32_e32 v176, -5, v175
	s_nop 0
	v_cndmask_b32_e32 v70, v165, v70, vcc
	v_cmp_lt_i32_e32 vcc, -1, v176
	s_nop 1
	v_cndmask_b32_e32 v87, v165, v87, vcc
	v_cmp_lt_i32_e32 vcc, 31, v176
	v_add_u32_e32 v176, -6, v175
	s_nop 0
	v_cndmask_b32_e32 v71, v165, v71, vcc
	v_cmp_lt_i32_e32 vcc, -1, v176
	s_nop 1
	v_cndmask_b32_e32 v88, v165, v88, vcc
	v_cmp_lt_i32_e32 vcc, 31, v176
	v_add_u32_e32 v176, -7, v175
	s_nop 0
	v_cndmask_b32_e32 v72, v165, v72, vcc
	v_cmp_lt_i32_e32 vcc, -1, v176
	s_nop 1
	v_cndmask_b32_e32 v89, v165, v89, vcc
	v_cmp_lt_i32_e32 vcc, 31, v176
	v_add_u32_e32 v176, -16, v175
	s_nop 0
	v_cndmask_b32_e32 v73, v165, v73, vcc
	v_cmp_lt_i32_e32 vcc, -1, v176
	s_nop 1
	v_cndmask_b32_e32 v90, v165, v90, vcc
	v_cmp_lt_i32_e32 vcc, 31, v176
	v_subrev_u32_e32 v176, 17, v175
	s_nop 0
	v_cndmask_b32_e32 v74, v165, v74, vcc
	v_cmp_lt_i32_e32 vcc, -1, v176
	s_nop 1
	v_cndmask_b32_e32 v91, v165, v91, vcc
	v_cmp_lt_i32_e32 vcc, 31, v176
	v_subrev_u32_e32 v176, 18, v175
	s_nop 0
	v_cndmask_b32_e32 v75, v165, v75, vcc
	v_cmp_lt_i32_e32 vcc, -1, v176
	s_nop 1
	v_cndmask_b32_e32 v92, v165, v92, vcc
	v_cmp_lt_i32_e32 vcc, 31, v176
	v_subrev_u32_e32 v176, 19, v175
	s_nop 0
	v_cndmask_b32_e32 v76, v165, v76, vcc
	v_cmp_lt_i32_e32 vcc, -1, v176
	s_nop 1
	v_cndmask_b32_e32 v93, v165, v93, vcc
	v_cmp_lt_i32_e32 vcc, 31, v176
	v_subrev_u32_e32 v176, 20, v175
	s_nop 0
	v_cndmask_b32_e32 v77, v165, v77, vcc
	v_cmp_lt_i32_e32 vcc, -1, v176
	s_nop 1
	v_cndmask_b32_e32 v94, v165, v94, vcc
	v_cmp_lt_i32_e32 vcc, 31, v176
	v_subrev_u32_e32 v176, 21, v175
	s_nop 0
	v_cndmask_b32_e32 v78, v165, v78, vcc
	v_cmp_lt_i32_e32 vcc, -1, v176
	s_nop 1
	v_cndmask_b32_e32 v95, v165, v95, vcc
	v_cmp_lt_i32_e32 vcc, 31, v176
	v_subrev_u32_e32 v176, 22, v175
	v_subrev_u32_e32 v175, 23, v175
	v_cndmask_b32_e32 v79, v165, v79, vcc
	v_cmp_lt_i32_e32 vcc, -1, v176
	s_nop 1
	v_cndmask_b32_e32 v96, v165, v96, vcc
	v_cmp_lt_i32_e32 vcc, 31, v176
	s_nop 1
	v_cndmask_b32_e32 v80, v165, v80, vcc
	v_cmp_lt_i32_e32 vcc, -1, v175
	s_nop 1
	v_cndmask_b32_e32 v97, v165, v97, vcc
	v_cmp_lt_i32_e32 vcc, 31, v175
	s_nop 1
	v_cndmask_b32_e32 v81, v165, v81, vcc

.LBB0_813:
	v_cvt_pk_bf16_f32 v178, v82, v175
	v_cvt_pk_bf16_f32 v179, v84, v85
	v_cvt_pk_bf16_f32 v180, v86, v87
	v_cvt_pk_bf16_f32 v181, v88, v176
	v_cvt_pk_bf16_f32 v84, v89, v90
	v_cvt_pk_bf16_f32 v85, v91, v92
	v_cvt_pk_bf16_f32 v86, v93, v94
	v_cvt_pk_bf16_f32 v87, v95, v96
	v_cvt_pk_bf16_f32 v66, v66, v67
	v_cvt_pk_bf16_f32 v67, v68, v69
	v_cvt_pk_bf16_f32 v68, v70, v71
	v_cvt_pk_bf16_f32 v69, v72, v83
	v_cvt_pk_bf16_f32 v70, v73, v74
	v_cvt_pk_bf16_f32 v71, v75, v76
	v_cvt_pk_bf16_f32 v72, v77, v78
	v_cvt_pk_bf16_f32 v73, v80, v81
	v_lshl_add_u32 v78, s87, 14, v172
	ds_read_b64_tr_b16 v[74:75], v78 offset:0
	ds_read_b64_tr_b16 v[76:77], v78 offset:0x800
	ds_read_b64_tr_b16 v[80:81], v78 offset:0x1000
	ds_read_b64_tr_b16 v[82:83], v78 offset:0x1800
	ds_read_b64_tr_b16 v[88:89], v78 offset:0x2000
	ds_read_b64_tr_b16 v[90:91], v78 offset:0x2800
	ds_read_b64_tr_b16 v[92:93], v78 offset:0x3000
	v_add_f32_e32 v79, v79, v177
	ds_read_b64_tr_b16 v[94:95], v78 offset:0x3800
	v_fmac_f32_e32 v79, v174, v97
	ds_read_b64_tr_b16 v[174:175], v78 offset:0x200
	ds_read_b64_tr_b16 v[176:177], v78 offset:0xa00
	ds_read_b64_tr_b16 v[182:183], v78 offset:0x1200
	ds_read_b64_tr_b16 v[184:185], v78 offset:0x1a00
	ds_read_b64_tr_b16 v[186:187], v78 offset:0x2200
	ds_read_b64_tr_b16 v[188:189], v78 offset:0x2a00
	ds_read_b64_tr_b16 v[190:191], v78 offset:0x3200
	ds_read_b64_tr_b16 v[192:193], v78 offset:0x3a00
	s_waitcnt lgkmcnt(8)


	v_mfma_f32_32x32x16_bf16 v[50:65], v[178:181], v[74:77], v[50:65]
	ds_read_b64_tr_b16 v[74:75], v78 offset:0x400
	ds_read_b64_tr_b16 v[76:77], v78 offset:0xc00
	v_mfma_f32_32x32x16_bf16 v[50:65], v[84:87], v[80:83], v[50:65]
	ds_read_b64_tr_b16 v[80:81], v78 offset:0x1400
	ds_read_b64_tr_b16 v[82:83], v78 offset:0x1c00
	v_mfma_f32_32x32x16_bf16 v[50:65], v[66:69], v[88:91], v[50:65]
	ds_read_b64_tr_b16 v[88:89], v78 offset:0x2400
	ds_read_b64_tr_b16 v[90:91], v78 offset:0x2c00
	v_mfma_f32_32x32x16_bf16 v[50:65], v[70:73], v[92:95], v[50:65]
	ds_read_b64_tr_b16 v[92:93], v78 offset:0x3400
	ds_read_b64_tr_b16 v[94:95], v78 offset:0x3c00
	s_waitcnt lgkmcnt(8)
	v_mfma_f32_32x32x16_bf16 v[34:49], v[178:181], v[174:177], v[34:49]
	ds_read_b64_tr_b16 v[174:175], v78 offset:0x600
	ds_read_b64_tr_b16 v[176:177], v78 offset:0xe00
	v_mfma_f32_32x32x16_bf16 v[34:49], v[84:87], v[182:185], v[34:49]
	ds_read_b64_tr_b16 v[182:183], v78 offset:0x1600
	ds_read_b64_tr_b16 v[184:185], v78 offset:0x1e00
	v_mfma_f32_32x32x16_bf16 v[34:49], v[66:69], v[186:189], v[34:49]
	ds_read_b64_tr_b16 v[186:187], v78 offset:0x2600
	ds_read_b64_tr_b16 v[188:189], v78 offset:0x2e00
	v_mfma_f32_32x32x16_bf16 v[34:49], v[70:73], v[190:193], v[34:49]
	ds_read_b64_tr_b16 v[190:191], v78 offset:0x3600
	ds_read_b64_tr_b16 v[192:193], v78 offset:0x3e00
	s_waitcnt lgkmcnt(8)
	v_mfma_f32_32x32x16_bf16 v[18:33], v[178:181], v[74:77], v[18:33]
	s_waitcnt lgkmcnt(0)
	v_mfma_f32_32x32x16_bf16 v[18:33], v[84:87], v[80:83], v[18:33]
	v_mfma_f32_32x32x16_bf16 v[18:33], v[66:69], v[88:91], v[18:33]
	v_mfma_f32_32x32x16_bf16 v[18:33], v[70:73], v[92:95], v[18:33]
	v_mfma_f32_32x32x16_bf16 v[2:17], v[178:181], v[174:177], v[2:17]
	s_add_i32 s86, s86, 64
	s_add_i32 s12, s12, 1
	s_add_u32 s94, s94, s16
	s_addc_u32 s95, s95, s17
	s_add_u32 s96, s96, s14
	s_addc_u32 s97, s97, s15


	v_mfma_f32_32x32x16_bf16 v[2:17], v[84:87], v[182:185], v[2:17]
	v_subrev_u32_e32 v168, 64, v168
	s_cmp_eq_u32 s83, s86
	v_mfma_f32_32x32x16_bf16 v[2:17], v[66:69], v[186:189], v[2:17]
	v_mfma_f32_32x32x16_bf16 v[2:17], v[70:73], v[190:193], v[2:17]
	s_cbranch_scc1 .LBB0_815
	v_mov_b32_e32 v174, v79
	s_add_i32 s56, s86, 0xe0
	s_cmp_ge_i32 s56, s84
	s_cbranch_scc0 .LBB0_805

.LBB0_945:
	s_or_b64 exec, exec, s[0:1]
	s_lshl_b32 s55, s80, 8
	s_and_b32 s0, s81, 15
	s_add_i32 s55, s55, s63
	s_lshl_b32 s54, s0, 8
	v_mov_b32_e32 v168, v1
	s_ashr_i32 s0, s55, 31
	s_add_u32 s52, s52, s55
	v_and_b32_e32 v167, 31, v168
	v_or_b32_e32 v30, s52, v167
	v_mov_b64_e32 v[2:3], s[6:7]
	s_addc_u32 s53, s53, s0
	v_mad_u64_u32 v[2:3], s[0:1], v30, s68, v[2:3]
	v_bfe_u32 v169, v168, 5, 1
	v_mad_i32_i24 v3, s53, v162, v3
	s_lshl_b32 s12, s82, 1
	v_lshl_add_u64 v[2:3], v[2:3], 0, s[12:13]
	v_lshlrev_b32_e32 v148, 4, v169
	v_lshl_add_u64 v[44:45], v[2:3], 0, v[148:149]
	global_load_dwordx4 v[32:35], v[44:45], off
	global_load_dwordx4 v[36:39], v[44:45], off offset:32
	global_load_dwordx4 v[26:29], v[44:45], off offset:64
	global_load_dwordx4 v[22:25], v[44:45], off offset:96
	global_load_dwordx4 v[18:21], v[44:45], off offset:128
	global_load_dwordx4 v[14:17], v[44:45], off offset:160
	global_load_dwordx4 v[10:13], v[44:45], off offset:192
	v_and_b32_e32 v118, 32, v168
	global_load_dwordx4 v[6:9], v118, s[4:5] offset:576
	s_waitcnt lgkmcnt(0)
	global_load_dwordx4 v[2:5], v118, s[4:5] offset:592
	global_load_dwordx4 v[102:105], v118, s[4:5] offset:704
	global_load_dwordx4 v[110:113], v118, s[4:5] offset:720
	global_load_dwordx4 v[40:43], v[44:45], off offset:224
	global_load_dwordx4 v[82:85], v[44:45], off offset:256
	global_load_dwordx4 v[138:141], v[44:45], off offset:288
	global_load_dwordx4 v[70:73], v[44:45], off offset:320
	global_load_dwordx4 v[142:145], v[44:45], off offset:352
	v_mov_b32_e32 v31, s53
	s_mov_b32 m0, s71
	s_mov_b32 s12, 1
	s_waitcnt vmcnt(0)
	v_and_b32_e32 v191, 0xffff0000, v32
	v_lshlrev_b32_e32 v190, 16, v32
	v_lshlrev_b32_e32 v206, 16, v26
	v_and_b32_e32 v207, 0xffff0000, v26
	v_lshlrev_b32_e32 v208, 16, v27
	v_and_b32_e32 v209, 0xffff0000, v27
	v_lshlrev_b32_e32 v210, 16, v28
	v_and_b32_e32 v211, 0xffff0000, v28
	v_lshlrev_b32_e32 v212, 16, v29
	v_and_b32_e32 v213, 0xffff0000, v29
	v_lshlrev_b32_e32 v222, 16, v18
	v_and_b32_e32 v223, 0xffff0000, v18
	v_lshlrev_b32_e32 v224, 16, v19
	v_and_b32_e32 v225, 0xffff0000, v19
	v_lshlrev_b32_e32 v226, 16, v20
	v_and_b32_e32 v227, 0xffff0000, v20
	v_lshlrev_b32_e32 v228, 16, v21
	v_and_b32_e32 v229, 0xffff0000, v21
	global_load_dwordx4 v[26:29], v118, s[4:5] offset:640
	global_load_dwordx4 v[156:159], v118, s[4:5] offset:656
	global_load_dwordx4 v[18:21], v118, s[4:5] offset:528
	v_mul_f32_e32 v188, v191, v191
	v_lshlrev_b32_e32 v192, 16, v33
	v_fmac_f32_e32 v188, v190, v190
	v_and_b32_e32 v193, 0xffff0000, v33
	v_fmac_f32_e32 v188, v192, v192
	v_lshlrev_b32_e32 v194, 16, v34
	v_fmac_f32_e32 v188, v193, v193
	v_and_b32_e32 v195, 0xffff0000, v34
	v_fmac_f32_e32 v188, v194, v194
	v_lshlrev_b32_e32 v196, 16, v35
	v_fmac_f32_e32 v188, v195, v195
	v_and_b32_e32 v197, 0xffff0000, v35
	v_fmac_f32_e32 v188, v196, v196
	v_lshlrev_b32_e32 v198, 16, v36
	v_fmac_f32_e32 v188, v197, v197
	v_and_b32_e32 v199, 0xffff0000, v36
	v_fmac_f32_e32 v188, v198, v198
	v_lshlrev_b32_e32 v200, 16, v37
	v_lshlrev_b32_e32 v214, 16, v22
	v_and_b32_e32 v215, 0xffff0000, v22
	v_lshlrev_b32_e32 v216, 16, v23
	v_and_b32_e32 v217, 0xffff0000, v23
	v_lshlrev_b32_e32 v218, 16, v24
	v_and_b32_e32 v219, 0xffff0000, v24
	v_lshlrev_b32_e32 v220, 16, v25
	v_and_b32_e32 v221, 0xffff0000, v25
	v_fmac_f32_e32 v188, v199, v199
	global_load_dwordx4 v[22:25], v118, s[4:5] offset:512
	v_and_b32_e32 v201, 0xffff0000, v37
	v_fmac_f32_e32 v188, v200, v200
	v_lshlrev_b32_e32 v202, 16, v38
	v_fmac_f32_e32 v188, v201, v201
	v_and_b32_e32 v203, 0xffff0000, v38
	v_fmac_f32_e32 v188, v202, v202
	v_lshlrev_b32_e32 v204, 16, v39
	v_fmac_f32_e32 v188, v203, v203
	v_and_b32_e32 v205, 0xffff0000, v39
	v_fmac_f32_e32 v188, v204, v204
	v_fmac_f32_e32 v188, v205, v205
	v_fmac_f32_e32 v188, v206, v206
	v_fmac_f32_e32 v188, v207, v207
	v_fmac_f32_e32 v188, v208, v208
	v_fmac_f32_e32 v188, v209, v209
	v_fmac_f32_e32 v188, v210, v210
	v_fmac_f32_e32 v188, v211, v211
	v_fmac_f32_e32 v188, v212, v212
	v_fmac_f32_e32 v188, v213, v213
	v_fmac_f32_e32 v188, v214, v214
	v_fmac_f32_e32 v188, v215, v215
	v_fmac_f32_e32 v188, v216, v216
	v_fmac_f32_e32 v188, v217, v217
	v_fmac_f32_e32 v188, v218, v218
	v_fmac_f32_e32 v188, v219, v219
	v_fmac_f32_e32 v188, v220, v220
	v_fmac_f32_e32 v188, v221, v221
	v_fmac_f32_e32 v188, v222, v222
	v_fmac_f32_e32 v188, v223, v223
	v_fmac_f32_e32 v188, v224, v224
	v_fmac_f32_e32 v188, v225, v225
	v_fmac_f32_e32 v188, v226, v226
	v_fmac_f32_e32 v188, v227, v227
	v_fmac_f32_e32 v188, v228, v228
	v_lshlrev_b32_e32 v230, 16, v14
	v_fmac_f32_e32 v188, v229, v229
	v_and_b32_e32 v231, 0xffff0000, v14
	v_fmac_f32_e32 v188, v230, v230
	v_lshlrev_b32_e32 v232, 16, v15
	v_fmac_f32_e32 v188, v231, v231
	v_and_b32_e32 v233, 0xffff0000, v15
	v_fmac_f32_e32 v188, v232, v232
	v_lshlrev_b32_e32 v234, 16, v16
	v_fmac_f32_e32 v188, v233, v233
	v_and_b32_e32 v235, 0xffff0000, v16
	v_fmac_f32_e32 v188, v234, v234
	v_lshlrev_b32_e32 v246, 16, v40
	v_and_b32_e32 v247, 0xffff0000, v40
	v_lshlrev_b32_e32 v248, 16, v41
	v_and_b32_e32 v249, 0xffff0000, v41
	v_lshlrev_b32_e32 v250, 16, v42
	v_and_b32_e32 v251, 0xffff0000, v42
	v_lshlrev_b32_e32 v252, 16, v43
	v_and_b32_e32 v253, 0xffff0000, v43
	global_load_dwordx4 v[106:109], v118, s[4:5] offset:16
	global_load_dwordx4 v[114:117], v118, s[4:5]
	global_load_dwordx4 v[94:97], v118, s[4:5] offset:80
	global_load_dwordx4 v[98:101], v118, s[4:5] offset:64
	global_load_dwordx4 v[86:89], v118, s[4:5] offset:144
	global_load_dwordx4 v[90:93], v118, s[4:5] offset:128
	global_load_dwordx4 v[74:77], v118, s[4:5] offset:208
	global_load_dwordx4 v[78:81], v118, s[4:5] offset:192
	global_load_dwordx4 v[62:65], v118, s[4:5] offset:272
	global_load_dwordx4 v[66:69], v118, s[4:5] offset:256
	global_load_dwordx4 v[54:57], v118, s[4:5] offset:336
	global_load_dwordx4 v[58:61], v118, s[4:5] offset:320
	global_load_dwordx4 v[46:49], v118, s[4:5] offset:400
	global_load_dwordx4 v[50:53], v118, s[4:5] offset:384
	global_load_dwordx4 v[38:41], v118, s[4:5] offset:464
	global_load_dwordx4 v[42:45], v118, s[4:5] offset:448
	v_lshlrev_b32_e32 v236, 16, v17
	v_fmac_f32_e32 v188, v235, v235
	v_and_b32_e32 v237, 0xffff0000, v17
	v_fmac_f32_e32 v188, v236, v236
	v_lshlrev_b32_e32 v238, 16, v10
	v_fmac_f32_e32 v188, v237, v237
	v_and_b32_e32 v239, 0xffff0000, v10
	v_fmac_f32_e32 v188, v238, v238
	v_lshlrev_b32_e32 v240, 16, v11
	v_fmac_f32_e32 v188, v239, v239
	v_and_b32_e32 v241, 0xffff0000, v11
	v_fmac_f32_e32 v188, v240, v240
	v_lshlrev_b32_e32 v242, 16, v12
	v_fmac_f32_e32 v188, v241, v241
	v_and_b32_e32 v243, 0xffff0000, v12
	v_fmac_f32_e32 v188, v242, v242
	v_lshlrev_b32_e32 v244, 16, v13
	v_fmac_f32_e32 v188, v243, v243
	v_and_b32_e32 v245, 0xffff0000, v13
	v_fmac_f32_e32 v188, v244, v244
	v_fmac_f32_e32 v188, v245, v245
	v_fmac_f32_e32 v188, v246, v246
	v_fmac_f32_e32 v188, v247, v247
	v_fmac_f32_e32 v188, v248, v248
	v_fmac_f32_e32 v188, v249, v249
	v_fmac_f32_e32 v188, v250, v250
	v_fmac_f32_e32 v188, v251, v251
	v_fmac_f32_e32 v188, v252, v252
	v_lshlrev_b32_e32 v187, 16, v82
	v_lshlrev_b32_e32 v186, 16, v70
	v_fmac_f32_e32 v188, v253, v253
	v_lshlrev_b32_e32 v124, 16, v144
	v_and_b32_e32 v126, 0xffff0000, v144
	v_lshlrev_b32_e32 v131, 16, v139
	v_and_b32_e32 v133, 0xffff0000, v139
	v_lshlrev_b32_e32 v137, 16, v138
	v_lshlrev_b32_e32 v136, 16, v142
	v_and_b32_e32 v139, 0xffff0000, v138
	v_and_b32_e32 v138, 0xffff0000, v142
	v_lshlrev_b32_e32 v142, 16, v73
	v_and_b32_e32 v144, 0xffff0000, v73
	v_lshlrev_b32_e32 v152, 16, v72
	v_and_b32_e32 v154, 0xffff0000, v72
	v_pk_mul_f32 v[72:73], v[186:187], v[186:187]
	s_waitcnt vmcnt(18)
	v_mov_b32_e32 v150, v158
	v_mov_b32_e32 v158, v156
	v_lshlrev_b32_e32 v156, 16, v71
	v_and_b32_e32 v184, 0xffff0000, v71
	v_and_b32_e32 v189, 0xffff0000, v82
	v_add_f32_e32 v71, v73, v188
	v_and_b32_e32 v188, 0xffff0000, v70
	v_mov_b32_e32 v128, v110
	v_mov_b32_e32 v129, v2
	v_mov_b32_e32 v2, v111
	s_waitcnt vmcnt(17)
	v_mov_b32_e32 v151, v20
	v_mov_b32_e32 v20, v159
	v_mov_b32_e32 v159, v18
	v_mov_b32_e32 v18, v157
	v_lshlrev_b32_e32 v157, 16, v83
	v_pk_mul_f32 v[110:111], v[188:189], v[188:189]
	v_lshlrev_b32_e32 v119, 16, v141
	v_and_b32_e32 v121, 0xffff0000, v141
	v_lshlrev_b32_e32 v125, 16, v140
	v_and_b32_e32 v127, 0xffff0000, v140
	v_mov_b32_e32 v140, v102
	v_mov_b32_e32 v141, v6
	v_mov_b32_e32 v6, v103
	v_pk_mul_f32 v[102:103], v[156:157], v[156:157]
	v_and_b32_e32 v185, 0xffff0000, v83
	v_add_f32_e32 v70, v111, v71
	v_mov_b32_e32 v134, v104
	v_mov_b32_e32 v135, v8
	v_mov_b32_e32 v8, v105
	v_lshlrev_b32_e32 v153, 16, v84
	v_pk_mul_f32 v[104:105], v[184:185], v[184:185]
	v_add_f32_e32 v70, v103, v70
	v_pk_mul_f32 v[180:181], v[152:153], v[152:153]
	v_and_b32_e32 v155, 0xffff0000, v84
	v_add_f32_e32 v70, v105, v70
	v_lshlrev_b32_e32 v130, 16, v143
	v_and_b32_e32 v132, 0xffff0000, v143
	v_lshlrev_b32_e32 v143, 16, v85
	v_pk_mul_f32 v[182:183], v[154:155], v[154:155]
	v_add_f32_e32 v70, v181, v70
	v_lshlrev_b32_e32 v118, 16, v145
	v_and_b32_e32 v120, 0xffff0000, v145
	v_pk_mul_f32 v[176:177], v[142:143], v[142:143]
	v_and_b32_e32 v145, 0xffff0000, v85
	v_add_f32_e32 v70, v183, v70
	v_pk_mul_f32 v[178:179], v[144:145], v[144:145]
	v_add_f32_e32 v70, v177, v70
	v_pk_mul_f32 v[172:173], v[136:137], v[136:137]
	v_add_f32_e32 v70, v179, v70
	v_pk_mul_f32 v[174:175], v[138:139], v[138:139]
	v_add_f32_e32 v70, v173, v70
	v_add_f32_e32 v70, v175, v70
	v_fmac_f32_e32 v70, v131, v131
	v_fmac_f32_e32 v70, v133, v133
	v_fmac_f32_e32 v70, v125, v125
	v_fmac_f32_e32 v70, v127, v127
	v_fmac_f32_e32 v70, v119, v119
	v_fmac_f32_e32 v70, v121, v121
	v_add_f32_e32 v103, v72, v70
	v_add_f32_e32 v103, v110, v103
	v_add_f32_e32 v102, v102, v103
	v_add_f32_e32 v173, v104, v102
	v_add_f32_e32 v173, v180, v173
	v_add_f32_e32 v173, v182, v173
	v_add_f32_e32 v173, v176, v173
	v_add_f32_e32 v173, v178, v173
	v_mov_b32_e32 v176, v132
	v_mov_b32_e32 v177, v130
	s_waitcnt vmcnt(16)
	v_mov_b32_e32 v179, v24
	v_add_f32_e32 v24, v172, v173
	v_lshlrev_b64 v[10:11], 8, v[30:31]
	v_pk_mul_f32 v[176:177], v[176:177], v[176:177]
	v_add_f32_e32 v24, v174, v24
	v_lshl_add_u64 v[10:11], s[10:11], 0, v[10:11]
	v_lshlrev_b32_e32 v12, 6, v169
	v_mov_b32_e32 v13, v149
	v_mov_b32_e32 v180, v126
	v_mov_b32_e32 v181, v124
	v_add_f32_e32 v24, v177, v24
	v_lshl_add_u64 v[170:171], v[10:11], 0, v[12:13]
	v_pk_mul_f32 v[180:181], v[180:181], v[180:181]
	v_add_f32_e32 v24, v176, v24
	global_load_dwordx4 v[10:13], v[170:171], off offset:48
	global_load_dwordx4 v[14:17], v[170:171], off offset:32
	global_load_dwordx4 v[30:33], v[170:171], off offset:16
	global_load_dwordx4 v[34:37], v[170:171], off
	v_mov_b32_e32 v122, v112
	v_mov_b32_e32 v123, v4
	v_mov_b32_e32 v4, v113
	global_load_dwordx4 v[70:73], v[170:171], off offset:176
	global_load_dwordx4 v[82:85], v[170:171], off offset:160
	global_load_dwordx4 v[102:105], v[170:171], off offset:144
	global_load_dwordx4 v[110:113], v[170:171], off offset:128
	v_mov_b32_e32 v170, v120
	v_mov_b32_e32 v171, v118
	v_add_f32_e32 v24, v181, v24
	v_pk_mul_f32 v[170:171], v[170:171], v[170:171]
	v_add_f32_e32 v24, v180, v24
	v_add_f32_e32 v24, v171, v24
	v_add_f32_e32 v24, v170, v24
	v_mov_b32_e32 v178, v28
	v_mov_b32_e32 v28, v24
	s_nop 1
	v_permlane32_swap_b32_e32 v24, v28
	v_add_f32_e32 v24, v24, v28
	v_fmamk_f32 v24, v24, 0x3baaaaab, v163
	v_mul_f32_e32 v28, 0x4b800000, v24
	v_cmp_gt_f32_e32 vcc, s69, v24
	s_nop 1
	v_cndmask_b32_e32 v24, v24, v28, vcc
	v_rsq_f32_e32 v170, v24
	v_mov_b32_e32 v24, v29
	v_mov_b32_e32 v29, v22
	v_mov_b32_e32 v28, v26
	v_mul_f32_e32 v22, 0x45800000, v170
	v_cndmask_b32_e32 v22, v170, v22, vcc
	v_mul_f32_e32 v26, 0x3dd53b94, v22
	s_waitcnt vmcnt(22)
	v_mul_f32_e32 v22, v114, v26
	v_mul_f32_e32 v114, v22, v190
	v_mul_f32_e32 v22, v106, v26
	v_mul_f32_e32 v106, v22, v194
	v_mul_f32_e32 v22, v115, v26
	v_mul_f32_e32 v115, v22, v191
	v_mul_f32_e32 v22, v107, v26
	v_mul_f32_e32 v107, v22, v195
	v_mul_f32_e32 v22, v116, v26
	v_mul_f32_e32 v116, v22, v192
	v_mul_f32_e32 v22, v108, v26
	v_mul_f32_e32 v108, v22, v196
	v_mul_f32_e32 v22, v117, v26
	v_mul_f32_e32 v117, v22, v193
	v_mul_f32_e32 v22, v109, v26
	v_mul_f32_e32 v109, v22, v197
	s_waitcnt vmcnt(20)
	v_mul_f32_e32 v22, v98, v26
	v_mul_f32_e32 v170, v22, v198
	v_mul_f32_e32 v22, v94, v26
	v_mul_f32_e32 v94, v22, v202
	v_mul_f32_e32 v22, v99, v26
	v_mul_f32_e32 v171, v22, v199
	v_mul_f32_e32 v22, v95, v26
	v_mul_f32_e32 v95, v22, v203
	v_mul_f32_e32 v22, v100, v26
	v_mul_f32_e32 v172, v22, v200
	v_mul_f32_e32 v22, v96, v26
	v_mul_f32_e32 v96, v22, v204
	v_mul_f32_e32 v22, v101, v26
	v_mul_f32_e32 v173, v22, v201
	v_mul_f32_e32 v22, v97, v26
	v_mul_f32_e32 v97, v22, v205
	s_waitcnt vmcnt(18)
	v_mul_f32_e32 v22, v90, v26
	v_mul_f32_e32 v90, v22, v206
	v_mul_f32_e32 v22, v86, v26
	v_mul_f32_e32 v86, v22, v210
	v_mul_f32_e32 v22, v91, v26
	v_mul_f32_e32 v91, v22, v207
	v_mul_f32_e32 v22, v87, v26
	v_mul_f32_e32 v87, v22, v211
	v_mul_f32_e32 v22, v92, v26
	v_mul_f32_e32 v92, v22, v208
	v_mul_f32_e32 v22, v88, v26
	v_mul_f32_e32 v88, v22, v212
	v_mul_f32_e32 v22, v93, v26
	v_mul_f32_e32 v93, v22, v209
	v_mul_f32_e32 v22, v89, v26
	v_mul_f32_e32 v89, v22, v213
	s_waitcnt vmcnt(16)
	v_mul_f32_e32 v22, v78, v26
	v_mul_f32_e32 v78, v22, v214
	v_mul_f32_e32 v22, v74, v26
	v_mul_f32_e32 v74, v22, v218
	v_mul_f32_e32 v22, v79, v26
	v_mul_f32_e32 v79, v22, v215
	v_mul_f32_e32 v22, v75, v26
	v_mul_f32_e32 v75, v22, v219
	v_mul_f32_e32 v22, v80, v26
	v_mul_f32_e32 v80, v22, v216
	v_mul_f32_e32 v22, v76, v26
	v_mul_f32_e32 v76, v22, v220
	v_mul_f32_e32 v22, v81, v26
	v_mul_f32_e32 v81, v22, v217
	v_mul_f32_e32 v22, v77, v26
	v_mul_f32_e32 v77, v22, v221
	s_waitcnt vmcnt(14)
	v_mul_f32_e32 v22, v66, v26
	v_mul_f32_e32 v66, v22, v222
	v_mul_f32_e32 v22, v26, v62
	v_mul_f32_e32 v62, v22, v226
	v_mul_f32_e32 v22, v67, v26
	v_mul_f32_e32 v67, v22, v223
	v_mul_f32_e32 v22, v26, v63
	v_mul_f32_e32 v63, v22, v227
	v_mul_f32_e32 v22, v68, v26
	v_mul_f32_e32 v68, v22, v224
	v_mul_f32_e32 v22, v26, v64
	v_mul_f32_e32 v64, v22, v228
	v_mul_f32_e32 v22, v69, v26
	v_mul_f32_e32 v69, v22, v225
	v_mul_f32_e32 v22, v26, v65
	v_mul_f32_e32 v65, v22, v229
	s_waitcnt vmcnt(12)
	v_mul_f32_e32 v22, v26, v58
	v_mul_f32_e32 v58, v22, v230
	v_mul_f32_e32 v22, v26, v54
	v_mul_f32_e32 v54, v22, v234
	v_mul_f32_e32 v22, v26, v59
	v_mul_f32_e32 v59, v22, v231
	v_mul_f32_e32 v22, v26, v55
	v_mul_f32_e32 v55, v22, v235
	v_mul_f32_e32 v22, v26, v60
	v_mul_f32_e32 v60, v22, v232
	v_mul_f32_e32 v22, v26, v56
	v_mul_f32_e32 v56, v22, v236
	v_mul_f32_e32 v22, v26, v61
	v_mul_f32_e32 v61, v22, v233
	v_mul_f32_e32 v22, v26, v57
	v_mul_f32_e32 v57, v22, v237
	s_waitcnt vmcnt(10)
	v_mul_f32_e32 v22, v26, v50
	v_mul_f32_e32 v174, v22, v238
	v_mul_f32_e32 v22, v26, v46
	v_mul_f32_e32 v175, v22, v242
	v_mul_f32_e32 v22, v26, v51
	v_mul_f32_e32 v176, v22, v239
	v_mul_f32_e32 v22, v26, v47
	v_mul_f32_e32 v177, v22, v243
	v_mul_f32_e32 v22, v26, v52
	v_mul_f32_e32 v52, v22, v240
	v_mul_f32_e32 v22, v26, v48
	v_mul_f32_e32 v180, v22, v244
	v_mul_f32_e32 v22, v26, v53
	v_mul_f32_e32 v53, v22, v241
	v_mul_f32_e32 v22, v26, v49
	v_mul_f32_e32 v181, v22, v245
	s_waitcnt vmcnt(8)
	v_mul_f32_e32 v22, v26, v42
	v_mul_f32_e32 v182, v22, v246
	v_mul_f32_e32 v22, v26, v38
	v_mul_f32_e32 v183, v22, v250
	v_mul_f32_e32 v22, v26, v43
	v_mul_f32_e32 v190, v22, v247
	v_mul_f32_e32 v22, v26, v39
	v_mul_f32_e32 v191, v22, v251
	v_mul_f32_e32 v22, v26, v44
	v_mul_f32_e32 v192, v22, v248
	v_mul_f32_e32 v22, v26, v40
	v_mul_f32_e32 v193, v22, v252
	v_mul_f32_e32 v22, v26, v45
	v_mul_f32_e32 v194, v22, v249
	v_mul_f32_e32 v22, v26, v41
	v_pk_mul_f32 v[28:29], v[26:27], v[28:29] op_sel_hi:[0,1]
	v_mul_f32_e32 v195, v22, v253
	v_pk_mul_f32 v[28:29], v[28:29], v[186:187]
	v_mov_b32_e32 v22, v27
	v_pk_mul_f32 v[38:39], v[26:27], v[158:159] op_sel_hi:[0,1]
	v_pk_mul_f32 v[22:23], v[26:27], v[22:23] op_sel_hi:[0,1]
	v_pk_mul_f32 v[18:19], v[26:27], v[18:19] op_sel_hi:[0,1]
	v_pk_mul_f32 v[40:41], v[26:27], v[178:179] op_sel_hi:[0,1]
	v_pk_mul_f32 v[42:43], v[26:27], v[150:151] op_sel_hi:[0,1]
	v_pk_mul_f32 v[24:25], v[26:27], v[24:25] op_sel_hi:[0,1]
	v_pk_mul_f32 v[20:21], v[26:27], v[20:21] op_sel_hi:[0,1]
	v_pk_mul_f32 v[44:45], v[26:27], v[140:141] op_sel_hi:[0,1]
	v_pk_mul_f32 v[46:47], v[26:27], v[128:129] op_sel_hi:[0,1]
	v_pk_mul_f32 v[6:7], v[26:27], v[6:7] op_sel_hi:[0,1]
	v_pk_mul_f32 v[2:3], v[26:27], v[2:3] op_sel_hi:[0,1]
	v_pk_mul_f32 v[48:49], v[26:27], v[134:135] op_sel_hi:[0,1]
	v_pk_mul_f32 v[50:51], v[26:27], v[122:123] op_sel_hi:[0,1]
	v_pk_mul_f32 v[8:9], v[26:27], v[8:9] op_sel_hi:[0,1]
	v_pk_mul_f32 v[4:5], v[26:27], v[4:5] op_sel_hi:[0,1]
	s_waitcnt vmcnt(4)
	v_pk_mul_f32 v[26:27], v[28:29], v[34:35] op_sel:[1,0] op_sel_hi:[0,1]
	v_pk_mul_f32 v[22:23], v[22:23], v[188:189]
	v_pk_mul_f32 v[48:49], v[48:49], v[130:131]
	v_sub_f32_e32 v130, v26, v27
	v_pk_mul_f32 v[26:27], v[28:29], v[34:35]
	v_pk_mul_f32 v[40:41], v[40:41], v[156:157]
	v_add_f32_e32 v28, v27, v26
	v_pk_mul_f32 v[26:27], v[22:23], v[36:37] op_sel:[1,0] op_sel_hi:[0,1]
	v_pk_mul_f32 v[22:23], v[22:23], v[36:37]
	v_sub_f32_e32 v26, v26, v27
	v_add_f32_e32 v27, v23, v22
	v_pk_mul_f32 v[22:23], v[40:41], v[30:31] op_sel:[1,0] op_sel_hi:[0,1]
	v_pk_mul_f32 v[24:25], v[24:25], v[184:185]
	v_sub_f32_e32 v29, v22, v23
	v_pk_mul_f32 v[22:23], v[40:41], v[30:31]
	v_pk_mul_f32 v[38:39], v[38:39], v[152:153]
	v_add_f32_e32 v30, v23, v22
	v_pk_mul_f32 v[22:23], v[24:25], v[32:33] op_sel:[1,0] op_sel_hi:[0,1]
	v_sub_f32_e32 v31, v22, v23
	v_pk_mul_f32 v[22:23], v[24:25], v[32:33]
	v_pk_mul_f32 v[18:19], v[18:19], v[154:155]
	v_add_f32_e32 v24, v23, v22
	v_pk_mul_f32 v[22:23], v[38:39], v[14:15] op_sel:[1,0] op_sel_hi:[0,1]
	v_pk_mul_f32 v[14:15], v[38:39], v[14:15]
	v_sub_f32_e32 v22, v22, v23
	v_add_f32_e32 v23, v15, v14
	v_pk_mul_f32 v[14:15], v[18:19], v[16:17] op_sel:[1,0] op_sel_hi:[0,1]
	v_pk_mul_f32 v[42:43], v[42:43], v[142:143]
	v_sub_f32_e32 v25, v14, v15
	v_pk_mul_f32 v[14:15], v[18:19], v[16:17]
	v_pk_mul_f32 v[20:21], v[20:21], v[144:145]
	v_add_f32_e32 v16, v15, v14
	v_pk_mul_f32 v[14:15], v[42:43], v[10:11] op_sel:[1,0] op_sel_hi:[0,1]
	v_pk_mul_f32 v[10:11], v[42:43], v[10:11]
	v_sub_f32_e32 v14, v14, v15
	v_add_f32_e32 v15, v11, v10
	v_pk_mul_f32 v[10:11], v[20:21], v[12:13] op_sel:[1,0] op_sel_hi:[0,1]
	v_pk_mul_f32 v[44:45], v[44:45], v[136:137]
	v_sub_f32_e32 v17, v10, v11
	v_pk_mul_f32 v[10:11], v[20:21], v[12:13]
	v_pk_mul_f32 v[6:7], v[6:7], v[138:139]
	v_add_f32_e32 v12, v11, v10
	s_waitcnt vmcnt(0)
	v_pk_mul_f32 v[10:11], v[44:45], v[110:111] op_sel:[1,0] op_sel_hi:[0,1]
	v_sub_f32_e32 v13, v10, v11
	v_pk_mul_f32 v[10:11], v[44:45], v[110:111]
	v_pk_mul_f32 v[8:9], v[8:9], v[132:133]
	v_add_f32_e32 v18, v11, v10
	v_pk_mul_f32 v[10:11], v[6:7], v[112:113] op_sel:[1,0] op_sel_hi:[0,1]
	v_pk_mul_f32 v[6:7], v[6:7], v[112:113]
	v_sub_f32_e32 v10, v10, v11
	v_add_f32_e32 v11, v7, v6
	v_pk_mul_f32 v[6:7], v[48:49], v[102:103] op_sel:[1,0] op_sel_hi:[0,1]
	v_sub_f32_e32 v19, v6, v7
	v_pk_mul_f32 v[6:7], v[48:49], v[102:103]
	v_pk_mul_f32 v[46:47], v[46:47], v[124:125]
	v_add_f32_e32 v20, v7, v6
	v_pk_mul_f32 v[6:7], v[8:9], v[104:105] op_sel:[1,0] op_sel_hi:[0,1]
	v_sub_f32_e32 v21, v6, v7
	v_pk_mul_f32 v[6:7], v[8:9], v[104:105]
	v_pk_mul_f32 v[2:3], v[2:3], v[126:127]
	v_add_f32_e32 v8, v7, v6
	v_pk_mul_f32 v[6:7], v[46:47], v[82:83] op_sel:[1,0] op_sel_hi:[0,1]
	v_sub_f32_e32 v9, v6, v7
	v_pk_mul_f32 v[6:7], v[46:47], v[82:83]
	v_pk_mul_f32 v[50:51], v[50:51], v[118:119]
	v_add_f32_e32 v32, v7, v6
	v_pk_mul_f32 v[6:7], v[2:3], v[84:85] op_sel:[1,0] op_sel_hi:[0,1]
	v_pk_mul_f32 v[2:3], v[2:3], v[84:85]
	v_sub_f32_e32 v6, v6, v7
	v_add_f32_e32 v7, v3, v2
	v_pk_mul_f32 v[2:3], v[50:51], v[70:71] op_sel:[1,0] op_sel_hi:[0,1]
	v_pk_mul_f32 v[4:5], v[4:5], v[120:121]
	v_sub_f32_e32 v33, v2, v3
	v_pk_mul_f32 v[2:3], v[50:51], v[70:71]
	v_cvt_pk_bf16_f32 v98, v114, v115
	v_cvt_pk_bf16_f32 v99, v116, v117
	v_cvt_pk_bf16_f32 v100, v106, v107
	v_cvt_pk_bf16_f32 v101, v108, v109
	v_cvt_pk_bf16_f32 v102, v170, v171
	s_nop 0
	v_add_f32_e32 v34, v3, v2
	v_pk_mul_f32 v[2:3], v[4:5], v[72:73] op_sel:[1,0] op_sel_hi:[0,1]
	v_sub_f32_e32 v35, v2, v3
	v_pk_mul_f32 v[2:3], v[4:5], v[72:73]
	v_cvt_pk_bf16_f32 v103, v172, v173
	v_cvt_pk_bf16_f32 v104, v94, v95
	v_cvt_pk_bf16_f32 v105, v96, v97
	v_cvt_pk_bf16_f32 v106, v90, v91
	v_cvt_pk_bf16_f32 v107, v92, v93
	s_nop 0
	v_add_f32_e32 v2, v3, v2
	v_cvt_pk_bf16_f32 v108, v86, v87
	v_cvt_pk_bf16_f32 v109, v88, v89
	v_cvt_pk_bf16_f32 v110, v78, v79
	v_cvt_pk_bf16_f32 v111, v80, v81
	v_cvt_pk_bf16_f32 v112, v74, v75
	v_cvt_pk_bf16_f32 v113, v76, v77
	v_cvt_pk_bf16_f32 v114, v66, v67
	v_cvt_pk_bf16_f32 v115, v68, v69
	v_cvt_pk_bf16_f32 v116, v62, v63
	v_cvt_pk_bf16_f32 v117, v64, v65
	v_cvt_pk_bf16_f32 v118, v58, v59
	v_cvt_pk_bf16_f32 v119, v60, v61
	v_cvt_pk_bf16_f32 v120, v54, v55
	v_cvt_pk_bf16_f32 v121, v56, v57
	v_cvt_pk_bf16_f32 v122, v174, v176
	v_cvt_pk_bf16_f32 v123, v52, v53
	v_cvt_pk_bf16_f32 v124, v175, v177
	v_cvt_pk_bf16_f32 v125, v180, v181
	v_cvt_pk_bf16_f32 v126, v182, v190
	v_cvt_pk_bf16_f32 v127, v192, v194
	v_cvt_pk_bf16_f32 v128, v183, v191
	v_cvt_pk_bf16_f32 v129, v193, v195
	v_cvt_pk_bf16_f32 v130, v130, v26
	v_cvt_pk_bf16_f32 v131, v29, v31
	v_cvt_pk_bf16_f32 v132, v22, v25
	v_cvt_pk_bf16_f32 v133, v14, v17
	v_cvt_pk_bf16_f32 v134, v13, v10
	v_cvt_pk_bf16_f32 v135, v19, v21
	v_cvt_pk_bf16_f32 v136, v9, v6
	v_cvt_pk_bf16_f32 v137, v33, v35
	v_cvt_pk_bf16_f32 v138, v28, v27
	v_cvt_pk_bf16_f32 v139, v30, v24
	v_cvt_pk_bf16_f32 v140, v23, v16
	v_cvt_pk_bf16_f32 v141, v15, v12
	v_cvt_pk_bf16_f32 v142, v18, v11
	v_cvt_pk_bf16_f32 v143, v20, v8
	v_cvt_pk_bf16_f32 v144, v32, v7
	v_cvt_pk_bf16_f32 v145, v34, v2
	v_mul_hi_i32 v2, v168, s70
	v_lshrrev_b32_e32 v3, 31, v2
	v_ashrrev_i32_e32 v2, 2, v2
	v_add_u32_e32 v2, v2, v3
	v_mul_lo_u32 v3, v2, 24
	v_sub_u32_e32 v3, v168, v3
	v_lshrrev_b32_e32 v16, 1, v2
	v_bitop3_b32 v3, v16, v3, 7 bitop3:0x6c
	v_mul_lo_u32 v2, v2, s68
	v_lshl_add_u32 v2, v3, 4, v2
	v_add_u32_e32 v3, 0x200, v168
	v_mul_hi_i32 v4, v3, s70
	v_lshrrev_b32_e32 v5, 31, v4
	v_ashrrev_i32_e32 v4, 2, v4
	v_add_u32_e32 v4, v4, v5
	v_mul_lo_u32 v5, v4, 24
	v_sub_u32_e32 v5, v3, v5
	v_lshrrev_b32_e32 v16, 1, v4
	v_bitop3_b32 v5, v16, v5, 7 bitop3:0x6c
	v_mul_lo_u32 v4, v4, s68
	v_lshl_add_u32 v4, v5, 4, v4
	v_add_u32_e32 v5, 0x400, v168
	v_mul_hi_i32 v6, v5, s70
	v_lshrrev_b32_e32 v7, 31, v6
	v_ashrrev_i32_e32 v6, 2, v6
	v_add_u32_e32 v6, v6, v7
	v_mul_lo_u32 v7, v6, 24
	v_sub_u32_e32 v5, v5, v7
	v_lshrrev_b32_e32 v16, 1, v6
	v_bitop3_b32 v5, v16, v5, 7 bitop3:0x6c
	v_mul_lo_u32 v6, v6, s68
	v_ashrrev_i32_e32 v9, 4, v168
	v_lshl_add_u32 v6, v5, 4, v6
	v_bfe_u32 v5, v168, 2, 2
	v_lshrrev_b32_e32 v7, 1, v168
	v_and_b32_e32 v10, 0x1ffff0, v9
	v_lshrrev_b32_e32 v9, 1, v9
	v_ashrrev_i32_e32 v3, 4, v3
	v_and_or_b32 v5, v7, 8, v5
	v_and_b32_e32 v7, 0x60, v168
	v_lshlrev_b32_e32 v8, 3, v168
	v_and_b32_e32 v9, 4, v9
	v_and_b32_e32 v11, 0x1ffff0, v3
	v_lshrrev_b32_e32 v3, 1, v3
	v_and_or_b32 v7, v8, 24, v7
	v_or3_b32 v9, v10, v9, v5
	v_and_b32_e32 v3, 4, v3
	s_barrier
	global_load_lds_dwordx4 v2, s[44:45]
	s_mov_b32 m0, s72
	v_lshlrev_b32_e32 v7, 1, v7
	v_lshlrev_b32_e32 v10, 11, v9
	v_or3_b32 v3, v11, v3, v5
	global_load_lds_dwordx4 v4, s[44:45]
	s_mov_b32 m0, s73
	v_or_b32_e32 v9, v10, v7
	v_lshlrev_b32_e32 v11, 11, v3
	global_load_lds_dwordx4 v6, s[44:45]
	s_mov_b32 m0, s64
	v_or_b32_e32 v3, v11, v7
	global_load_lds_dwordx4 v9, s[46:47]
	s_mov_b32 m0, s74
	v_lshlrev_b32_e32 v13, 1, v168
	global_load_lds_dwordx4 v3, s[46:47]
	v_lshlrev_b32_e32 v9, 4, v168
	v_and_b32_e32 v14, 32, v13
	v_or_b32_e32 v3, 32, v148
	v_and_b32_e32 v16, 0x13, v167
	v_and_b32_e32 v17, 4, v167
	v_lshl_or_b32 v16, v17, 1, v16
	v_and_b32_e32 v17, 8, v167
	v_lshrrev_b32_e32 v17, 1, v17
	v_or_b32_e32 v16, v16, v17
	v_mul_u32_u24_e32 v5, 0x180, v16
	v_lshlrev_b32_e32 v17, 3, v16
	v_and_b32_e32 v7, 0x70, v17
	v_and_b32_e32 v12, 0xc0, v9
	v_and_or_b32 v8, v8, s75, v14
	v_bitop3_b32 v172, v3, v5, v7 bitop3:0xde
	v_or_b32_e32 v3, 64, v148
	v_mul_i32_i24_e32 v15, -8, v169
	v_add3_u32 v169, v12, 0, v8
	v_and_b32_e32 v12, 0xc0, v13
	v_and_b32_e32 v13, 48, v9
	v_bitop3_b32 v173, v3, v5, v7 bitop3:0xde
	v_or_b32_e32 v3, 0x60, v148
	v_or3_b32 v8, v11, v12, v13
	v_mov_b32_e32 v9, v149
	v_bitop3_b32 v171, v148, v5, v7 bitop3:0xde
	v_bitop3_b32 v174, v3, v5, v7 bitop3:0xde
	v_mov_b32_e32 v3, v149
	v_mov_b32_e32 v5, v149
	v_mov_b32_e32 v7, v149
	v_lshl_add_u64 v[150:151], s[48:49], 0, v[8:9]
	v_mov_b32_e32 v240, v8
	v_or3_b32 v8, v10, v12, v13
	v_mov_b32_e32 v16, v149
	v_mov_b32_e32 v17, v149
	v_and_b32_e32 v170, 63, v168
	s_lshl_b32 s46, s80, 2
	v_lshl_add_u32 v168, v167, 2, s65
	v_lshl_add_u64 v[152:153], s[48:49], 0, v[8:9]
	v_mov_b32_e32 v241, v8
	v_lshl_add_u64 v[154:155], s[50:51], 0, v[6:7]
	v_mov_b32_e32 v242, v6
	v_lshl_add_u64 v[156:157], s[50:51], 0, v[4:5]
	v_mov_b32_e32 v243, v4
	v_lshl_add_u64 v[158:159], s[50:51], 0, v[2:3]
	v_mov_b32_e32 v244, v2
	s_add_u32 s94, s2, s50
	s_addc_u32 s95, s3, s51
	s_add_u32 s96, s2, s48
	s_addc_u32 s97, s3, s49
	v_add3_u32 v167, s63, v15, v167
	v_mov_b32_e32 v2, v149
	v_mov_b32_e32 v4, v149
	v_mov_b32_e32 v6, v149
	v_mov_b32_e32 v8, v149
	v_mov_b32_e32 v10, v149
	v_mov_b32_e32 v11, v149
	v_mov_b32_e32 v12, v149
	v_mov_b32_e32 v13, v149
	v_mov_b32_e32 v14, v149
	v_mov_b32_e32 v15, v149
	v_mov_b64_e32 v[32:33], v[16:17]
	v_mov_b64_e32 v[48:49], v[16:17]
	v_mov_b64_e32 v[64:65], v[16:17]
	s_add_i32 s46, s46, 4
	v_cmp_gt_u32_e64 s[0:1], 32, v170
	v_mov_b32_e32 v176, 0
	v_mov_b32_e32 v175, 0
	v_mov_b32_e32 v210, 0
	v_mov_b32_e32 v211, 0
	v_mov_b32_e32 v212, 0
	v_mov_b32_e32 v213, 0
	v_mov_b32_e32 v214, 0
	v_mov_b32_e32 v215, 0
	v_mov_b32_e32 v216, 0
	v_mov_b32_e32 v217, 0
	v_mov_b32_e32 v218, 0
	v_mov_b32_e32 v219, 0
	v_mov_b32_e32 v220, 0
	v_mov_b32_e32 v221, 0
	v_mov_b32_e32 v222, 0
	v_mov_b32_e32 v223, 0
	v_mov_b32_e32 v224, 0
	v_mov_b32_e32 v225, 0
	s_movk_i32 s47, 0xff00
	v_mov_b64_e32 v[30:31], v[14:15]
	v_mov_b64_e32 v[28:29], v[12:13]
	v_mov_b64_e32 v[26:27], v[10:11]
	v_mov_b64_e32 v[24:25], v[8:9]
	v_mov_b64_e32 v[22:23], v[6:7]
	v_mov_b64_e32 v[20:21], v[4:5]
	v_mov_b64_e32 v[18:19], v[2:3]
	v_mov_b64_e32 v[46:47], v[14:15]
	v_mov_b64_e32 v[44:45], v[12:13]
	v_mov_b64_e32 v[42:43], v[10:11]
	v_mov_b64_e32 v[40:41], v[8:9]
	v_mov_b64_e32 v[38:39], v[6:7]
	v_mov_b64_e32 v[36:37], v[4:5]
	v_mov_b64_e32 v[34:35], v[2:3]
	v_mov_b64_e32 v[62:63], v[14:15]
	v_mov_b64_e32 v[60:61], v[12:13]
	v_mov_b64_e32 v[58:59], v[10:11]
	v_mov_b64_e32 v[56:57], v[8:9]
	v_mov_b64_e32 v[54:55], v[6:7]
	v_mov_b64_e32 v[52:53], v[4:5]
	v_mov_b64_e32 v[50:51], v[2:3]

.LBB0_948:
	s_mul_i32 s44, s48, 0x6000
	s_add_i32 s44, s44, 0
	s_add_i32 s44, s44, 0x8000
	v_add_u32_e32 v177, s44, v171
	ds_read_b128 v[66:69], v177 offset:0
	ds_read_b128 v[82:85], v177 offset:0x3000
	v_add_u32_e32 v206, s44, v172
	ds_read_b128 v[178:181], v206 offset:0
	ds_read_b128 v[182:185], v206 offset:0x3000
	v_add_u32_e32 v207, s44, v173
	ds_read_b128 v[186:189], v207 offset:0
	ds_read_b128 v[190:193], v207 offset:0x3000
	s_waitcnt lgkmcnt(4)
	v_add_u32_e32 v208, s44, v174
	v_mfma_f32_32x32x16_bf16 v[66:81], v[66:69], v[98:101], v[210:225]
	ds_read_b128 v[194:197], v208 offset:0
	ds_read_b128 v[198:201], v208 offset:0x3000
	s_waitcnt lgkmcnt(4)
	v_mfma_f32_32x32x16_bf16 v[82:97], v[82:85], v[98:101], v[210:225]
	v_mfma_f32_32x32x16_bf16 v[66:81], v[178:181], v[102:105], v[66:81]
	ds_read_b128 v[178:181], v177 offset:0x80
	ds_read_b128 v[202:205], v177 offset:0x3080
	s_waitcnt lgkmcnt(4)
	v_mfma_f32_32x32x16_bf16 v[82:97], v[182:185], v[102:105], v[82:97]
	v_mfma_f32_32x32x16_bf16 v[66:81], v[186:189], v[106:109], v[66:81]
	ds_read_b128 v[182:185], v206 offset:0x80
	ds_read_b128 v[186:189], v206 offset:0x3080
	s_waitcnt lgkmcnt(4)
	v_mfma_f32_32x32x16_bf16 v[82:97], v[190:193], v[106:109], v[82:97]
	v_mfma_f32_32x32x16_bf16 v[66:81], v[194:197], v[110:113], v[66:81]
	ds_read_b128 v[190:193], v207 offset:0x80
	ds_read_b128 v[194:197], v207 offset:0x3080
	s_waitcnt lgkmcnt(4)
	v_mfma_f32_32x32x16_bf16 v[82:97], v[198:201], v[110:113], v[82:97]
	v_mfma_f32_32x32x16_bf16 v[66:81], v[178:181], v[114:117], v[66:81]
	ds_read_b128 v[178:181], v208 offset:0x80
	ds_read_b128 v[198:201], v208 offset:0x3080
	s_waitcnt lgkmcnt(4)
	v_mfma_f32_32x32x16_bf16 v[82:97], v[202:205], v[114:117], v[82:97]
	v_mfma_f32_32x32x16_bf16 v[66:81], v[182:185], v[118:121], v[66:81]
	ds_read_b128 v[182:185], v177 offset:0x100
	ds_read_b128 v[202:205], v177 offset:0x3100
	s_waitcnt lgkmcnt(4)
	v_mfma_f32_32x32x16_bf16 v[82:97], v[186:189], v[118:121], v[82:97]
	v_mfma_f32_32x32x16_bf16 v[66:81], v[190:193], v[122:125], v[66:81]
	ds_read_b128 v[186:189], v206 offset:0x100
	ds_read_b128 v[190:193], v206 offset:0x3100
	s_waitcnt lgkmcnt(4)
	v_mfma_f32_32x32x16_bf16 v[82:97], v[194:197], v[122:125], v[82:97]
	v_mfma_f32_32x32x16_bf16 v[66:81], v[178:181], v[126:129], v[66:81]
	ds_read_b128 v[178:181], v207 offset:0x100
	ds_read_b128 v[194:197], v207 offset:0x3100
	s_waitcnt lgkmcnt(4)
	v_mfma_f32_32x32x16_bf16 v[82:97], v[198:201], v[126:129], v[82:97]
	v_mfma_f32_32x32x16_bf16 v[66:81], v[182:185], v[130:133], v[66:81]
	ds_read_b128 v[182:185], v208 offset:0x100
	ds_read_b128 v[198:201], v208 offset:0x3100
	s_waitcnt lgkmcnt(4)
	v_mfma_f32_32x32x16_bf16 v[82:97], v[202:205], v[130:133], v[82:97]
	v_mfma_f32_32x32x16_bf16 v[66:81], v[186:189], v[134:137], v[66:81]
	s_waitcnt lgkmcnt(2)
	v_mfma_f32_32x32x16_bf16 v[82:97], v[190:193], v[134:137], v[82:97]
	v_mfma_f32_32x32x16_bf16 v[66:81], v[178:181], v[138:141], v[66:81]
	s_waitcnt lgkmcnt(0)
	v_mfma_f32_32x32x16_bf16 v[82:97], v[194:197], v[138:141], v[82:97]
	v_mfma_f32_32x32x16_bf16 v[66:81], v[182:185], v[142:145], v[66:81]
	s_add_i32 s44, s47, 0x13f
	s_cmp_le_i32 s44, s55
	v_mfma_f32_32x32x16_bf16 v[82:97], v[198:201], v[142:145], v[82:97]
	s_cbranch_scc1 .LBB0_950
	v_add_u32_e32 v177, s54, v167
	v_cmp_lt_i32_e32 vcc, -1, v177
	v_add_u32_e32 v178, -1, v177
	s_nop 4
	v_cndmask_b32_e32 v66, v165, v66, vcc
	v_cmp_lt_i32_e32 vcc, 31, v177
	s_nop 1
	v_cndmask_b32_e32 v82, v165, v82, vcc
	v_cmp_lt_i32_e32 vcc, -1, v178
	s_nop 1
	v_cndmask_b32_e32 v67, v165, v67, vcc
	v_cmp_lt_i32_e32 vcc, 31, v178
	v_add_u32_e32 v178, -2, v177
	s_nop 0
	v_cndmask_b32_e32 v83, v165, v83, vcc
	v_cmp_lt_i32_e32 vcc, -1, v178
	s_nop 1
	v_cndmask_b32_e32 v68, v165, v68, vcc
	v_cmp_lt_i32_e32 vcc, 31, v178
	v_add_u32_e32 v178, -3, v177
	s_nop 0
	v_cndmask_b32_e32 v84, v165, v84, vcc
	v_cmp_lt_i32_e32 vcc, -1, v178
	s_nop 1
	v_cndmask_b32_e32 v69, v165, v69, vcc
	v_cmp_lt_i32_e32 vcc, 31, v178
	v_add_u32_e32 v178, -4, v177
	s_nop 0
	v_cndmask_b32_e32 v85, v165, v85, vcc
	v_cmp_lt_i32_e32 vcc, -1, v178
	s_nop 1
	v_cndmask_b32_e32 v70, v165, v70, vcc
	v_cmp_lt_i32_e32 vcc, 31, v178
	v_add_u32_e32 v178, -5, v177
	s_nop 0
	v_cndmask_b32_e32 v86, v165, v86, vcc
	v_cmp_lt_i32_e32 vcc, -1, v178
	s_nop 1
	v_cndmask_b32_e32 v71, v165, v71, vcc
	v_cmp_lt_i32_e32 vcc, 31, v178
	v_add_u32_e32 v178, -6, v177
	s_nop 0
	v_cndmask_b32_e32 v87, v165, v87, vcc
	v_cmp_lt_i32_e32 vcc, -1, v178
	s_nop 1
	v_cndmask_b32_e32 v72, v165, v72, vcc
	v_cmp_lt_i32_e32 vcc, 31, v178
	v_add_u32_e32 v178, -7, v177
	s_nop 0
	v_cndmask_b32_e32 v88, v165, v88, vcc
	v_cmp_lt_i32_e32 vcc, -1, v178
	s_nop 1
	v_cndmask_b32_e32 v73, v165, v73, vcc
	v_cmp_lt_i32_e32 vcc, 31, v178
	v_add_u32_e32 v178, -16, v177
	s_nop 0
	v_cndmask_b32_e32 v89, v165, v89, vcc
	v_cmp_lt_i32_e32 vcc, -1, v178
	s_nop 1
	v_cndmask_b32_e32 v74, v165, v74, vcc
	v_cmp_lt_i32_e32 vcc, 31, v178
	v_subrev_u32_e32 v178, 17, v177
	s_nop 0
	v_cndmask_b32_e32 v90, v165, v90, vcc
	v_cmp_lt_i32_e32 vcc, -1, v178
	s_nop 1
	v_cndmask_b32_e32 v75, v165, v75, vcc
	v_cmp_lt_i32_e32 vcc, 31, v178
	v_subrev_u32_e32 v178, 18, v177
	s_nop 0
	v_cndmask_b32_e32 v91, v165, v91, vcc
	v_cmp_lt_i32_e32 vcc, -1, v178
	s_nop 1
	v_cndmask_b32_e32 v76, v165, v76, vcc
	v_cmp_lt_i32_e32 vcc, 31, v178
	v_subrev_u32_e32 v178, 19, v177
	s_nop 0
	v_cndmask_b32_e32 v92, v165, v92, vcc
	v_cmp_lt_i32_e32 vcc, -1, v178
	s_nop 1
	v_cndmask_b32_e32 v77, v165, v77, vcc
	v_cmp_lt_i32_e32 vcc, 31, v178
	v_subrev_u32_e32 v178, 20, v177
	s_nop 0
	v_cndmask_b32_e32 v93, v165, v93, vcc
	v_cmp_lt_i32_e32 vcc, -1, v178
	s_nop 1
	v_cndmask_b32_e32 v78, v165, v78, vcc
	v_cmp_lt_i32_e32 vcc, 31, v178
	v_subrev_u32_e32 v178, 21, v177
	s_nop 0
	v_cndmask_b32_e32 v94, v165, v94, vcc
	v_cmp_lt_i32_e32 vcc, -1, v178
	s_nop 1
	v_cndmask_b32_e32 v79, v165, v79, vcc
	v_cmp_lt_i32_e32 vcc, 31, v178
	v_subrev_u32_e32 v178, 22, v177
	v_subrev_u32_e32 v177, 23, v177
	v_cndmask_b32_e32 v95, v165, v95, vcc
	v_cmp_lt_i32_e32 vcc, -1, v178
	s_nop 1
	v_cndmask_b32_e32 v80, v165, v80, vcc
	v_cmp_lt_i32_e32 vcc, 31, v178
	s_nop 1
	v_cndmask_b32_e32 v96, v165, v96, vcc
	v_cmp_lt_i32_e32 vcc, -1, v177
	s_nop 1
	v_cndmask_b32_e32 v81, v165, v81, vcc
	v_cmp_lt_i32_e32 vcc, 31, v177
	s_nop 1
	v_cndmask_b32_e32 v97, v165, v97, vcc

.LBB0_954:
	v_add_f32_e32 v81, v81, v97
	v_fmac_f32_e32 v81, v176, v96
	v_cvt_pk_bf16_f32 v176, v177, v178
	v_cvt_pk_bf16_f32 v177, v83, v84
	v_cvt_pk_bf16_f32 v178, v85, v86
	v_cvt_pk_bf16_f32 v179, v87, v179
	v_cvt_pk_bf16_f32 v84, v88, v89
	v_cvt_pk_bf16_f32 v85, v90, v91
	v_cvt_pk_bf16_f32 v86, v92, v93
	v_cvt_pk_bf16_f32 v87, v94, v95
	v_cvt_pk_bf16_f32 v66, v66, v67
	v_cvt_pk_bf16_f32 v67, v68, v69
	v_cvt_pk_bf16_f32 v68, v70, v71
	v_cvt_pk_bf16_f32 v69, v72, v82
	v_cvt_pk_bf16_f32 v70, v73, v74
	v_cvt_pk_bf16_f32 v71, v75, v76
	v_cvt_pk_bf16_f32 v72, v77, v78
	v_cvt_pk_bf16_f32 v73, v79, v80
	v_lshl_add_u32 v78, s48, 14, v169
	ds_read_b64_tr_b16 v[74:75], v78 offset:0
	ds_read_b64_tr_b16 v[76:77], v78 offset:0x800
	ds_read_b64_tr_b16 v[88:89], v78 offset:0x1000
	ds_read_b64_tr_b16 v[90:91], v78 offset:0x1800
	ds_read_b64_tr_b16 v[92:93], v78 offset:0x2000
	ds_read_b64_tr_b16 v[94:95], v78 offset:0x2800
	ds_read_b64_tr_b16 v[180:181], v78 offset:0x3000
	ds_read_b64_tr_b16 v[182:183], v78 offset:0x3800
	ds_read_b64_tr_b16 v[184:185], v78 offset:0x200
	ds_read_b64_tr_b16 v[186:187], v78 offset:0xa00
	ds_read_b64_tr_b16 v[188:189], v78 offset:0x1200
	ds_read_b64_tr_b16 v[190:191], v78 offset:0x1a00
	ds_read_b64_tr_b16 v[192:193], v78 offset:0x2200
	ds_read_b64_tr_b16 v[194:195], v78 offset:0x2a00
	ds_read_b64_tr_b16 v[196:197], v78 offset:0x3200
	ds_read_b64_tr_b16 v[198:199], v78 offset:0x3a00
	s_waitcnt lgkmcnt(8)


	v_mfma_f32_32x32x16_bf16 v[50:65], v[176:179], v[74:77], v[50:65]
	ds_read_b64_tr_b16 v[74:75], v78 offset:0x400
	ds_read_b64_tr_b16 v[76:77], v78 offset:0xc00
	v_mfma_f32_32x32x16_bf16 v[50:65], v[84:87], v[88:91], v[50:65]
	ds_read_b64_tr_b16 v[88:89], v78 offset:0x1400
	ds_read_b64_tr_b16 v[90:91], v78 offset:0x1c00
	v_mfma_f32_32x32x16_bf16 v[50:65], v[66:69], v[92:95], v[50:65]
	ds_read_b64_tr_b16 v[92:93], v78 offset:0x2400
	ds_read_b64_tr_b16 v[94:95], v78 offset:0x2c00
	ds_read_b64_tr_b16 v[200:201], v78 offset:0x3400
	ds_read_b64_tr_b16 v[202:203], v78 offset:0x3c00
	s_waitcnt lgkmcnt(8)
	v_mfma_f32_32x32x16_bf16 v[50:65], v[70:73], v[180:183], v[50:65]
	v_mfma_f32_32x32x16_bf16 v[34:49], v[176:179], v[184:187], v[34:49]
	ds_read_b64_tr_b16 v[180:181], v78 offset:0x600
	ds_read_b64_tr_b16 v[182:183], v78 offset:0xe00
	ds_read_b64_tr_b16 v[184:185], v78 offset:0x1600
	ds_read_b64_tr_b16 v[186:187], v78 offset:0x1e00
	v_mfma_f32_32x32x16_bf16 v[34:49], v[84:87], v[188:191], v[34:49]
	ds_read_b64_tr_b16 v[188:189], v78 offset:0x2600
	ds_read_b64_tr_b16 v[190:191], v78 offset:0x2e00
	v_mfma_f32_32x32x16_bf16 v[34:49], v[66:69], v[192:195], v[34:49]
	ds_read_b64_tr_b16 v[192:193], v78 offset:0x3600
	ds_read_b64_tr_b16 v[194:195], v78 offset:0x3e00
	s_waitcnt lgkmcnt(8)
	v_mfma_f32_32x32x16_bf16 v[34:49], v[70:73], v[196:199], v[34:49]
	v_mfma_f32_32x32x16_bf16 v[18:33], v[176:179], v[74:77], v[18:33]
	s_waitcnt lgkmcnt(0)
	v_mfma_f32_32x32x16_bf16 v[18:33], v[84:87], v[88:91], v[18:33]
	v_mfma_f32_32x32x16_bf16 v[18:33], v[66:69], v[92:95], v[18:33]
	v_mfma_f32_32x32x16_bf16 v[18:33], v[70:73], v[200:203], v[18:33]
	v_mfma_f32_32x32x16_bf16 v[2:17], v[176:179], v[180:183], v[2:17]
	s_add_i32 s47, s47, 64
	s_add_i32 s12, s12, 1
	s_add_u32 s94, s94, s16
	s_addc_u32 s95, s95, s17
	s_add_u32 s96, s96, s14
	s_addc_u32 s97, s97, s15


	v_mfma_f32_32x32x16_bf16 v[2:17], v[84:87], v[184:187], v[2:17]
	v_subrev_u32_e32 v167, 64, v167
	s_cmp_eq_u32 s54, s47
	v_mfma_f32_32x32x16_bf16 v[2:17], v[66:69], v[188:191], v[2:17]
	v_mfma_f32_32x32x16_bf16 v[2:17], v[70:73], v[192:195], v[2:17]
	s_cbranch_scc1 .LBB0_956
	v_mov_b32_e32 v176, v81
	s_add_i32 s44, s47, 0xe0
	s_cmp_ge_i32 s44, s55
	s_cbranch_scc0 .LBB0_946
